# v39 plus every group of eight scaled MFMA instructions aligned to 16 bytes (fetch alignment check)
# baseline (speedup 1.0000x reference)
.LBB0_194:
	s_add_u32 s34, s92, 0xfffa0080
	s_addc_u32 s35, s93, -1
	s_add_i32 s2, 0, 0x10000
	s_cmp_eq_u32 s1, 12
	s_cselect_b32 s95, s57, s35
	s_cselect_b32 s94, vcc_lo, s34
	s_cselect_b32 s97, s55, s11
	v_add_u32_e32 v146, s68, v174
	s_cselect_b32 s96, vcc_hi, s10
	s_add_i32 s82, 0, 0x14000
	v_add_u32_e32 v142, s2, v146
	v_add_u32_e32 v159, s82, v146
	ds_read_b128 v[130:133], v142
	ds_read_b128 v[134:137], v142 offset:1024
	ds_read_b128 v[138:141], v142 offset:2048
	ds_read_b128 v[142:145], v142 offset:3072
	ds_read_b128 v[146:149], v159
	ds_read_b128 v[150:153], v159 offset:1024
	ds_read_b128 v[160:163], v159 offset:2048
	ds_read_b128 v[164:167], v159 offset:3072
	v_add_u32_e32 v159, s69, v174
	s_mov_b32 s34, 0xfffe0000
	ds_read_b128 v[176:179], v159
	ds_read_b128 v[180:183], v159 offset:1024
	ds_read_b128 v[184:187], v159 offset:2048
	ds_read_b128 v[188:191], v159 offset:3072
	ds_read_b128 v[196:199], v159 offset:4096
	ds_read_b128 v[200:203], v159 offset:5120
	ds_read_b128 v[204:207], v159 offset:6144
	ds_read_b128 v[208:211], v159 offset:7168
	s_mov_b32 s35, -1
	v_lshl_add_u64 v[168:169], s[92:93], 0, v[154:155]
	v_lshl_add_u64 v[168:169], v[168:169], 0, s[34:35]
	s_add_i32 m0, s89, 0xc000
	s_nop 0
	global_load_lds_dwordx4 v[168:169], off
	s_add_i32 m0, s89, 0xe000
	s_nop 0
	global_load_lds_dwordx4 v154, s[92:93]
	s_waitcnt vmcnt(8)
	s_waitcnt lgkmcnt(0)
	s_barrier
	s_setprio 1
	s_waitcnt lgkmcnt(0)
	.p2align	4
	v_mfma_scale_f32_16x16x128_f8f6f4 v[126:129], v[130:137], v[176:183], v[126:129], v1, v1 op_sel_hi:[0,0,0]
	v_mfma_scale_f32_16x16x128_f8f6f4 v[122:125], v[138:145], v[176:183], v[122:125], v1, v1 op_sel_hi:[0,0,0]
	v_mfma_scale_f32_16x16x128_f8f6f4 v[114:117], v[130:137], v[184:191], v[114:117], v1, v1 op_sel_hi:[0,0,0]
	v_mfma_scale_f32_16x16x128_f8f6f4 v[106:109], v[138:145], v[184:191], v[106:109], v1, v1 op_sel_hi:[0,0,0]
	v_mfma_scale_f32_16x16x128_f8f6f4 v[98:101], v[130:137], v[196:203], v[98:101], v1, v1 op_sel_hi:[0,0,0]
	v_mfma_scale_f32_16x16x128_f8f6f4 v[212:215], v[138:145], v[196:203], v[90:93], v1, v1 op_sel_hi:[0,0,0]
	v_mfma_scale_f32_16x16x128_f8f6f4 v[216:219], v[130:137], v[204:211], v[82:85], v1, v1 op_sel_hi:[0,0,0]
	v_mfma_scale_f32_16x16x128_f8f6f4 v[220:223], v[138:145], v[204:211], v[74:77], v1, v1 op_sel_hi:[0,0,0]
	s_setprio 0
	s_setprio 1
	.p2align	4
	v_mfma_scale_f32_16x16x128_f8f6f4 v[118:121], v[146:153], v[176:183], v[118:121], v1, v1 op_sel_hi:[0,0,0]
	v_mfma_scale_f32_16x16x128_f8f6f4 v[110:113], v[160:167], v[176:183], v[110:113], v1, v1 op_sel_hi:[0,0,0]
	v_mfma_scale_f32_16x16x128_f8f6f4 v[102:105], v[146:153], v[184:191], v[102:105], v1, v1 op_sel_hi:[0,0,0]
	v_mfma_scale_f32_16x16x128_f8f6f4 v[176:179], v[160:167], v[184:191], v[94:97], v1, v1 op_sel_hi:[0,0,0]
	v_mfma_scale_f32_16x16x128_f8f6f4 v[180:183], v[146:153], v[196:203], v[86:89], v1, v1 op_sel_hi:[0,0,0]
	v_mfma_scale_f32_16x16x128_f8f6f4 v[184:187], v[160:167], v[196:203], v[78:81], v1, v1 op_sel_hi:[0,0,0]
	v_mfma_scale_f32_16x16x128_f8f6f4 v[188:191], v[146:153], v[204:211], v[62:65], v1, v1 op_sel_hi:[0,0,0]
	v_mfma_scale_f32_16x16x128_f8f6f4 v[196:199], v[160:167], v[204:211], v[58:61], v1, v1 op_sel_hi:[0,0,0]
	s_setprio 0
	s_barrier
	v_mov_b32_e32 v159, v155
	v_add_u32_e32 v94, s69, v174
	s_add_i32 s2, s2, s6
	s_nop 1
	ds_read_b128 v[58:61], v94 offset:16384
	ds_read_b128 v[62:65], v94 offset:17408
	ds_read_b128 v[74:77], v94 offset:18432
	ds_read_b128 v[78:81], v94 offset:19456
	ds_read_b128 v[82:85], v94 offset:20480
	ds_read_b128 v[86:89], v94 offset:21504
	ds_read_b128 v[90:93], v94 offset:22528
	ds_read_b128 v[94:97], v94 offset:23552
	s_mov_b32 m0, s2
	v_lshl_add_u64 v[168:169], s[96:97], 0, v[158:159]
	global_load_lds_dwordx4 v158, s[96:97]
	v_lshl_add_u64 v[168:169], v[168:169], 0, s[14:15]
	s_add_i32 m0, s2, 0x2000
	s_add_i32 s2, s82, s6
	global_load_lds_dwordx4 v[168:169], off
	s_mov_b32 m0, s2
	v_lshl_add_u64 v[168:169], s[96:97], 0, v[158:159]
	v_lshl_add_u64 v[170:171], v[168:169], 0, s[16:17]
	global_load_lds_dwordx4 v[170:171], off
	v_lshl_add_u64 v[168:169], v[168:169], 0, s[18:19]
	s_add_i32 m0, s2, 0x2000
	s_nop 0
	global_load_lds_dwordx4 v[168:169], off
	s_mov_b32 m0, s89
	v_lshl_add_u64 v[168:169], s[94:95], 0, v[154:155]
	global_load_lds_dwordx4 v154, s[94:95]
	v_lshl_add_u64 v[168:169], v[168:169], 0, s[14:15]
	s_mov_b32 m0, s91
	s_nop 0
	global_load_lds_dwordx4 v[168:169], off
	s_waitcnt vmcnt(8)
	s_waitcnt lgkmcnt(0)
	s_barrier
	s_setprio 1
	s_waitcnt lgkmcnt(0)
	.p2align	4
	v_mfma_scale_f32_16x16x128_f8f6f4 v[54:57], v[130:137], v[58:65], v[54:57], v1, v1 op_sel_hi:[0,0,0]
	v_mfma_scale_f32_16x16x128_f8f6f4 v[200:203], v[138:145], v[58:65], v[42:45], v1, v1 op_sel_hi:[0,0,0]
	v_mfma_scale_f32_16x16x128_f8f6f4 v[204:207], v[130:137], v[74:81], v[30:33], v1, v1 op_sel_hi:[0,0,0]
	v_mfma_scale_f32_16x16x128_f8f6f4 v[208:211], v[138:145], v[74:81], v[26:29], v1, v1 op_sel_hi:[0,0,0]
	v_mfma_scale_f32_16x16x128_f8f6f4 v[224:227], v[130:137], v[82:89], v[14:17], v1, v1 op_sel_hi:[0,0,0]
	v_mfma_scale_f32_16x16x128_f8f6f4 v[228:231], v[138:145], v[82:89], v[10:13], v1, v1 op_sel_hi:[0,0,0]
	v_mfma_scale_f32_16x16x128_f8f6f4 v[232:235], v[130:137], v[90:97], v[6:9], v1, v1 op_sel_hi:[0,0,0]
	v_mfma_scale_f32_16x16x128_f8f6f4 v[236:239], v[138:145], v[90:97], v[2:5], v1, v1 op_sel_hi:[0,0,0]
	s_setprio 0
	s_setprio 1
	.p2align	4
	v_mfma_scale_f32_16x16x128_f8f6f4 v[66:69], v[146:153], v[58:65], v[66:69], v1, v1 op_sel_hi:[0,0,0]
	v_mfma_scale_f32_16x16x128_f8f6f4 v[70:73], v[160:167], v[58:65], v[70:73], v1, v1 op_sel_hi:[0,0,0]
	v_mfma_scale_f32_16x16x128_f8f6f4 v[50:53], v[160:167], v[74:81], v[50:53], v1, v1 op_sel_hi:[0,0,0]
	v_mfma_scale_f32_16x16x128_f8f6f4 v[240:243], v[146:153], v[74:81], v[46:49], v1, v1 op_sel_hi:[0,0,0]
	v_mfma_scale_f32_16x16x128_f8f6f4 v[244:247], v[146:153], v[82:89], v[34:37], v1, v1 op_sel_hi:[0,0,0]
	v_mfma_scale_f32_16x16x128_f8f6f4 v[248:251], v[160:167], v[82:89], v[38:41], v1, v1 op_sel_hi:[0,0,0]
	v_mfma_scale_f32_16x16x128_f8f6f4 v[192:195], v[146:153], v[90:97], v[18:21], v1, v1 op_sel_hi:[0,0,0]
	v_mfma_scale_f32_16x16x128_f8f6f4 v[168:171], v[160:167], v[90:97], v[22:25], v1, v1 op_sel_hi:[0,0,0]
	s_setprio 0
	s_barrier
	s_add_i32 s2, 0, 0x18000
	v_add_u32_e32 v10, s68, v174
	s_add_i32 s34, 0, 0x1c000
	v_add_u32_e32 v11, s2, v10
	v_add_u32_e32 v10, s34, v10
	ds_read_b128 v[2:5], v11
	ds_read_b128 v[6:9], v11 offset:1024
	ds_read_b128 v[18:21], v11 offset:2048
	ds_read_b128 v[22:25], v11 offset:3072
	ds_read_b128 v[130:133], v10
	ds_read_b128 v[134:137], v10 offset:1024
	ds_read_b128 v[138:141], v10 offset:2048
	ds_read_b128 v[142:145], v10 offset:3072
	v_add_u32_e32 v46, s69, v174
	ds_read_b128 v[10:13], v46 offset:32768
	ds_read_b128 v[14:17], v46 offset:33792
	ds_read_b128 v[26:29], v46 offset:34816
	ds_read_b128 v[30:33], v46 offset:35840
	ds_read_b128 v[34:37], v46 offset:36864
	ds_read_b128 v[38:41], v46 offset:37888
	ds_read_b128 v[42:45], v46 offset:38912
	ds_read_b128 v[46:49], v46 offset:39936
	s_mov_b32 m0, s7
	v_lshl_add_u64 v[58:59], s[94:95], 0, v[154:155]
	v_lshl_add_u64 v[60:61], v[58:59], 0, s[16:17]
	global_load_lds_dwordx4 v[60:61], off
	v_lshl_add_u64 v[58:59], v[58:59], 0, s[18:19]
	s_mov_b32 m0, s0
	s_nop 0
	global_load_lds_dwordx4 v[58:59], off
	s_waitcnt vmcnt(8)
	s_waitcnt lgkmcnt(0)
	s_barrier
	s_setprio 1
	s_waitcnt lgkmcnt(0)
	.p2align	4
	v_mfma_scale_f32_16x16x128_f8f6f4 v[126:129], v[2:9], v[10:17], v[126:129], v1, v1 op_sel_hi:[0,0,0]
	v_mfma_scale_f32_16x16x128_f8f6f4 v[122:125], v[18:25], v[10:17], v[122:125], v1, v1 op_sel_hi:[0,0,0]
	v_mfma_scale_f32_16x16x128_f8f6f4 v[114:117], v[2:9], v[26:33], v[114:117], v1, v1 op_sel_hi:[0,0,0]
	v_mfma_scale_f32_16x16x128_f8f6f4 v[106:109], v[18:25], v[26:33], v[106:109], v1, v1 op_sel_hi:[0,0,0]
	v_mfma_scale_f32_16x16x128_f8f6f4 v[98:101], v[2:9], v[34:41], v[98:101], v1, v1 op_sel_hi:[0,0,0]
	v_mfma_scale_f32_16x16x128_f8f6f4 v[90:93], v[18:25], v[34:41], v[212:215], v1, v1 op_sel_hi:[0,0,0]
	v_mfma_scale_f32_16x16x128_f8f6f4 v[82:85], v[2:9], v[42:49], v[216:219], v1, v1 op_sel_hi:[0,0,0]
	v_mfma_scale_f32_16x16x128_f8f6f4 v[74:77], v[18:25], v[42:49], v[220:223], v1, v1 op_sel_hi:[0,0,0]
	s_setprio 0
	s_setprio 1
	.p2align	4
	v_mfma_scale_f32_16x16x128_f8f6f4 v[118:121], v[130:137], v[10:17], v[118:121], v1, v1 op_sel_hi:[0,0,0]
	v_mfma_scale_f32_16x16x128_f8f6f4 v[110:113], v[138:145], v[10:17], v[110:113], v1, v1 op_sel_hi:[0,0,0]
	v_mfma_scale_f32_16x16x128_f8f6f4 v[102:105], v[130:137], v[26:33], v[102:105], v1, v1 op_sel_hi:[0,0,0]
	v_mfma_scale_f32_16x16x128_f8f6f4 v[94:97], v[138:145], v[26:33], v[176:179], v1, v1 op_sel_hi:[0,0,0]
	v_mfma_scale_f32_16x16x128_f8f6f4 v[86:89], v[130:137], v[34:41], v[180:183], v1, v1 op_sel_hi:[0,0,0]
	v_mfma_scale_f32_16x16x128_f8f6f4 v[78:81], v[138:145], v[34:41], v[184:187], v1, v1 op_sel_hi:[0,0,0]
	v_mfma_scale_f32_16x16x128_f8f6f4 v[62:65], v[130:137], v[42:49], v[188:191], v1, v1 op_sel_hi:[0,0,0]
	v_mfma_scale_f32_16x16x128_f8f6f4 v[58:61], v[138:145], v[42:49], v[196:199], v1, v1 op_sel_hi:[0,0,0]
	s_setprio 0
	s_barrier
	s_add_i32 s2, s2, s6
	v_add_u32_e32 v10, s69, v174
	ds_read_b128 v[34:37], v10 offset:49152
	ds_read_b128 v[38:41], v10 offset:50176
	ds_read_b128 v[146:149], v10 offset:51200
	ds_read_b128 v[150:153], v10 offset:52224
	ds_read_b128 v[160:163], v10 offset:53248
	ds_read_b128 v[164:167], v10 offset:54272
	ds_read_b128 v[176:179], v10 offset:55296
	ds_read_b128 v[180:183], v10 offset:56320
	s_mov_b32 m0, s2
	v_lshl_add_u64 v[10:11], s[96:97], 0, v[158:159]
	v_lshl_add_u64 v[12:13], v[10:11], 0, s[20:21]
	global_load_lds_dwordx4 v[12:13], off
	v_lshl_add_u64 v[10:11], v[10:11], 0, s[22:23]
	s_add_i32 m0, s2, 0x2000
	s_add_i32 s2, s34, s6
	global_load_lds_dwordx4 v[10:11], off
	s_mov_b32 m0, s2
	v_lshl_add_u64 v[10:11], s[96:97], 0, v[158:159]
	v_lshl_add_u64 v[12:13], v[10:11], 0, s[24:25]
	global_load_lds_dwordx4 v[12:13], off
	v_lshl_add_u64 v[10:11], v[10:11], 0, s[26:27]
	s_add_i32 m0, s2, 0x2000
	s_nop 0
	global_load_lds_dwordx4 v[10:11], off
	s_mov_b32 m0, s33
	v_lshl_add_u64 v[10:11], s[94:95], 0, v[154:155]
	v_lshl_add_u64 v[12:13], v[10:11], 0, s[20:21]
	global_load_lds_dwordx4 v[12:13], off
	v_lshl_add_u64 v[10:11], v[10:11], 0, s[22:23]
	s_mov_b32 m0, s76
	s_nop 0
	global_load_lds_dwordx4 v[10:11], off
	s_waitcnt vmcnt(8)
	s_waitcnt lgkmcnt(0)
	s_barrier
	s_setprio 1
	s_waitcnt lgkmcnt(0)
	.p2align	4
	v_mfma_scale_f32_16x16x128_f8f6f4 v[54:57], v[2:9], v[34:41], v[54:57], v1, v1 op_sel_hi:[0,0,0]
	v_mfma_scale_f32_16x16x128_f8f6f4 v[42:45], v[18:25], v[34:41], v[200:203], v1, v1 op_sel_hi:[0,0,0]
	v_mfma_scale_f32_16x16x128_f8f6f4 v[30:33], v[2:9], v[146:153], v[204:207], v1, v1 op_sel_hi:[0,0,0]
	v_mfma_scale_f32_16x16x128_f8f6f4 v[26:29], v[18:25], v[146:153], v[208:211], v1, v1 op_sel_hi:[0,0,0]
	v_mfma_scale_f32_16x16x128_f8f6f4 v[14:17], v[2:9], v[160:167], v[224:227], v1, v1 op_sel_hi:[0,0,0]
	v_mfma_scale_f32_16x16x128_f8f6f4 v[10:13], v[18:25], v[160:167], v[228:231], v1, v1 op_sel_hi:[0,0,0]
	v_mfma_scale_f32_16x16x128_f8f6f4 v[6:9], v[2:9], v[176:183], v[232:235], v1, v1 op_sel_hi:[0,0,0]
	v_mfma_scale_f32_16x16x128_f8f6f4 v[2:5], v[18:25], v[176:183], v[236:239], v1, v1 op_sel_hi:[0,0,0]
	s_setprio 0
	s_setprio 1
	.p2align	4
	v_mfma_scale_f32_16x16x128_f8f6f4 v[66:69], v[130:137], v[34:41], v[66:69], v1, v1 op_sel_hi:[0,0,0]
	v_mfma_scale_f32_16x16x128_f8f6f4 v[70:73], v[138:145], v[34:41], v[70:73], v1, v1 op_sel_hi:[0,0,0]
	v_mfma_scale_f32_16x16x128_f8f6f4 v[46:49], v[130:137], v[146:153], v[240:243], v1, v1 op_sel_hi:[0,0,0]
	v_mfma_scale_f32_16x16x128_f8f6f4 v[50:53], v[138:145], v[146:153], v[50:53], v1, v1 op_sel_hi:[0,0,0]
	v_mfma_scale_f32_16x16x128_f8f6f4 v[34:37], v[130:137], v[160:167], v[244:247], v1, v1 op_sel_hi:[0,0,0]
	v_mfma_scale_f32_16x16x128_f8f6f4 v[38:41], v[138:145], v[160:167], v[248:251], v1, v1 op_sel_hi:[0,0,0]
	v_mfma_scale_f32_16x16x128_f8f6f4 v[18:21], v[130:137], v[176:183], v[192:195], v1, v1 op_sel_hi:[0,0,0]
	v_mfma_scale_f32_16x16x128_f8f6f4 v[22:25], v[138:145], v[176:183], v[168:171], v1, v1 op_sel_hi:[0,0,0]
	s_setprio 0
	s_barrier
	s_add_i32 s1, s1, 2
	s_add_u32 s92, s92, 0x100
	s_addc_u32 s93, s93, 0
	s_add_u32 s10, s10, 0x100
	s_addc_u32 s11, s11, 0
	s_cmp_gt_u32 s1, 13
	s_cbranch_scc0 .LBB0_194
	s_and_b64 vcc, exec, s[64:65]
	s_cbranch_vccz .LBB0_197
	s_barrier

.LBB0_977:
	s_add_u32 s34, s58, 0xfffd0080
	v_add_u32_e32 v46, s84, v1
	v_add_u32_e32 v47, s88, v46
	v_add_u32_e32 v46, s89, v46
	ds_read_b128 v[130:133], v47
	ds_read_b128 v[134:137], v47 offset:1024
	ds_read_b128 v[138:141], v47 offset:2048
	ds_read_b128 v[142:145], v47 offset:3072
	ds_read_b128 v[146:149], v46
	ds_read_b128 v[150:153], v46 offset:1024
	ds_read_b128 v[154:157], v46 offset:2048
	ds_read_b128 v[158:161], v46 offset:3072
	s_addc_u32 s35, s59, -1
	s_cmp_eq_u32 s70, 4
	s_cselect_b32 s61, s38, s35
	s_cselect_b32 s60, s39, s34
	s_cselect_b32 s63, s45, s69
	s_cselect_b32 s62, s47, s68
	v_add_u32_e32 v46, s85, v1
	s_mov_b32 s34, 0xffff0000
	ds_read_b128 v[162:165], v46
	ds_read_b128 v[166:169], v46 offset:1024
	ds_read_b128 v[170:173], v46 offset:2048
	ds_read_b128 v[174:177], v46 offset:3072
	ds_read_b128 v[178:181], v46 offset:4096
	ds_read_b128 v[182:185], v46 offset:5120
	ds_read_b128 v[186:189], v46 offset:6144
	ds_read_b128 v[190:193], v46 offset:7168
	s_mov_b32 s35, -1
	v_lshl_add_u64 v[46:47], s[58:59], 0, v[196:197]
	v_lshl_add_u64 v[46:47], v[46:47], 0, s[34:35]
	s_add_i32 m0, s64, 0xc000
	s_nop 0
	global_load_lds_dwordx4 v[46:47], off
	s_add_i32 m0, s64, 0xe000
	s_nop 0
	global_load_lds_dwordx4 v196, s[58:59]
	s_waitcnt vmcnt(8)
	s_waitcnt lgkmcnt(0)
	s_barrier
	s_setprio 1
	s_waitcnt lgkmcnt(0)
	.p2align	4
	v_mfma_scale_f32_16x16x128_f8f6f4 v[94:97], v[130:137], v[162:169], v[94:97], v195, v195 op_sel_hi:[0,0,0]
	v_mfma_scale_f32_16x16x128_f8f6f4 v[90:93], v[138:145], v[162:169], v[90:93], v195, v195 op_sel_hi:[0,0,0]
	v_mfma_scale_f32_16x16x128_f8f6f4 v[86:89], v[130:137], v[170:177], v[86:89], v195, v195 op_sel_hi:[0,0,0]
	v_mfma_scale_f32_16x16x128_f8f6f4 v[82:85], v[138:145], v[170:177], v[82:85], v195, v195 op_sel_hi:[0,0,0]
	v_mfma_scale_f32_16x16x128_f8f6f4 v[78:81], v[130:137], v[178:185], v[78:81], v195, v195 op_sel_hi:[0,0,0]
	v_mfma_scale_f32_16x16x128_f8f6f4 v[204:207], v[138:145], v[178:185], v[74:77], v195, v195 op_sel_hi:[0,0,0]
	v_mfma_scale_f32_16x16x128_f8f6f4 v[208:211], v[130:137], v[186:193], v[70:73], v195, v195 op_sel_hi:[0,0,0]
	v_mfma_scale_f32_16x16x128_f8f6f4 v[212:215], v[138:145], v[186:193], v[66:69], v195, v195 op_sel_hi:[0,0,0]
	s_setprio 0
	s_setprio 1
	.p2align	4
	v_mfma_scale_f32_16x16x128_f8f6f4 v[38:41], v[154:161], v[178:185], v[38:41], v195, v195 op_sel_hi:[0,0,0]
	v_mfma_scale_f32_16x16x128_f8f6f4 v[216:219], v[146:153], v[162:169], v[62:65], v195, v195 op_sel_hi:[0,0,0]
	v_mfma_scale_f32_16x16x128_f8f6f4 v[162:165], v[154:161], v[162:169], v[58:61], v195, v195 op_sel_hi:[0,0,0]
	v_mfma_scale_f32_16x16x128_f8f6f4 v[166:169], v[146:153], v[170:177], v[54:57], v195, v195 op_sel_hi:[0,0,0]
	v_mfma_scale_f32_16x16x128_f8f6f4 v[170:173], v[154:161], v[170:177], v[14:17], v195, v195 op_sel_hi:[0,0,0]
	v_mfma_scale_f32_16x16x128_f8f6f4 v[174:177], v[146:153], v[178:185], v[10:13], v195, v195 op_sel_hi:[0,0,0]
	v_mfma_scale_f32_16x16x128_f8f6f4 v[178:181], v[146:153], v[186:193], v[30:33], v195, v195 op_sel_hi:[0,0,0]
	v_mfma_scale_f32_16x16x128_f8f6f4 v[182:185], v[154:161], v[186:193], v[22:25], v195, v195 op_sel_hi:[0,0,0]
	s_setprio 0
	s_barrier
	v_mov_b32_e32 v203, v197
	s_nop 1
	v_add_u32_e32 v10, s85, v1
	s_add_i32 s34, s88, s43
	ds_read_b128 v[46:49], v10 offset:16384
	ds_read_b128 v[50:53], v10 offset:17408
	ds_read_b128 v[54:57], v10 offset:18432
	ds_read_b128 v[58:61], v10 offset:19456
	ds_read_b128 v[62:65], v10 offset:20480
	ds_read_b128 v[66:69], v10 offset:21504
	ds_read_b128 v[70:73], v10 offset:22528
	ds_read_b128 v[74:77], v10 offset:23552
	s_mov_b32 m0, s34
	v_lshl_add_u64 v[10:11], s[62:63], 0, v[202:203]
	global_load_lds_dwordx4 v202, s[62:63]
	v_lshl_add_u64 v[10:11], v[10:11], 0, s[12:13]
	s_add_i32 m0, s34, 0x2000
	s_add_i32 s34, s89, s43
	global_load_lds_dwordx4 v[10:11], off
	s_mov_b32 m0, s34
	v_lshl_add_u64 v[10:11], s[62:63], 0, v[202:203]
	v_lshl_add_u64 v[12:13], v[10:11], 0, s[14:15]
	global_load_lds_dwordx4 v[12:13], off
	v_lshl_add_u64 v[10:11], v[10:11], 0, s[16:17]
	s_add_i32 m0, s34, 0x2000
	s_nop 0
	global_load_lds_dwordx4 v[10:11], off
	s_mov_b32 m0, s64
	v_lshl_add_u64 v[10:11], s[60:61], 0, v[196:197]
	global_load_lds_dwordx4 v196, s[60:61]
	v_lshl_add_u64 v[10:11], v[10:11], 0, s[12:13]
	s_mov_b32 m0, s65
	s_nop 0
	global_load_lds_dwordx4 v[10:11], off
	s_waitcnt vmcnt(8)
	s_waitcnt lgkmcnt(0)
	s_barrier
	s_setprio 1
	s_waitcnt lgkmcnt(0)
	.p2align	4
	v_mfma_scale_f32_16x16x128_f8f6f4 v[42:45], v[130:137], v[46:53], v[42:45], v195, v195 op_sel_hi:[0,0,0]
	v_mfma_scale_f32_16x16x128_f8f6f4 v[34:37], v[138:145], v[46:53], v[34:37], v195, v195 op_sel_hi:[0,0,0]
	v_mfma_scale_f32_16x16x128_f8f6f4 v[224:227], v[130:137], v[62:69], v[224:227], v195, v195 op_sel_hi:[0,0,0]
	v_mfma_scale_f32_16x16x128_f8f6f4 v[228:231], v[138:145], v[62:69], v[228:231], v195, v195 op_sel_hi:[0,0,0]
	v_mfma_scale_f32_16x16x128_f8f6f4 v[186:189], v[130:137], v[54:61], v[26:29], v195, v195 op_sel_hi:[0,0,0]
	v_mfma_scale_f32_16x16x128_f8f6f4 v[190:193], v[138:145], v[54:61], v[18:21], v195, v195 op_sel_hi:[0,0,0]
	v_mfma_scale_f32_16x16x128_f8f6f4 v[232:235], v[130:137], v[70:77], v[6:9], v195, v195 op_sel_hi:[0,0,0]
	v_mfma_scale_f32_16x16x128_f8f6f4 v[236:239], v[138:145], v[70:77], v[2:5], v195, v195 op_sel_hi:[0,0,0]
	s_setprio 0
	s_setprio 1
	.p2align	4
	v_mfma_scale_f32_16x16x128_f8f6f4 v[240:243], v[146:153], v[46:53], v[98:101], v195, v195 op_sel_hi:[0,0,0]
	v_mfma_scale_f32_16x16x128_f8f6f4 v[244:247], v[154:161], v[46:53], v[102:105], v195, v195 op_sel_hi:[0,0,0]
	v_mfma_scale_f32_16x16x128_f8f6f4 v[248:251], v[146:153], v[54:61], v[106:109], v195, v195 op_sel_hi:[0,0,0]
	v_mfma_scale_f32_16x16x128_f8f6f4 v[198:201], v[154:161], v[54:61], v[110:113], v195, v195 op_sel_hi:[0,0,0]
	v_mfma_scale_f32_16x16x128_f8f6f4 v[220:223], v[146:153], v[62:69], v[114:117], v195, v195 op_sel_hi:[0,0,0]
	v_mfma_scale_f32_16x16x128_f8f6f4 v[46:49], v[154:161], v[62:69], v[118:121], v195, v195 op_sel_hi:[0,0,0]
	v_mfma_scale_f32_16x16x128_f8f6f4 v[50:53], v[146:153], v[70:77], v[122:125], v195, v195 op_sel_hi:[0,0,0]
	v_mfma_scale_f32_16x16x128_f8f6f4 v[154:157], v[154:161], v[70:77], v[126:129], v195, v195 op_sel_hi:[0,0,0]
	s_setprio 0
	s_barrier
	s_add_i32 s34, 0, 0x18000
	v_add_u32_e32 v10, s84, v1
	s_add_i32 s35, 0, 0x1c000
	v_add_u32_e32 v11, s34, v10
	v_add_u32_e32 v10, s35, v10
	ds_read_b128 v[2:5], v11
	ds_read_b128 v[6:9], v11 offset:1024
	ds_read_b128 v[98:101], v11 offset:2048
	ds_read_b128 v[102:105], v11 offset:3072
	ds_read_b128 v[122:125], v10
	ds_read_b128 v[126:129], v10 offset:1024
	ds_read_b128 v[130:133], v10 offset:2048
	ds_read_b128 v[134:137], v10 offset:3072
	v_add_u32_e32 v54, s85, v1
	ds_read_b128 v[10:13], v54 offset:32768
	ds_read_b128 v[14:17], v54 offset:33792
	ds_read_b128 v[18:21], v54 offset:34816
	ds_read_b128 v[22:25], v54 offset:35840
	ds_read_b128 v[26:29], v54 offset:36864
	ds_read_b128 v[30:33], v54 offset:37888
	ds_read_b128 v[106:109], v54 offset:38912
	ds_read_b128 v[110:113], v54 offset:39936
	s_mov_b32 m0, s66
	v_lshl_add_u64 v[54:55], s[60:61], 0, v[196:197]
	v_lshl_add_u64 v[56:57], v[54:55], 0, s[14:15]
	global_load_lds_dwordx4 v[56:57], off
	v_lshl_add_u64 v[54:55], v[54:55], 0, s[16:17]
	s_mov_b32 m0, s67
	s_nop 0
	global_load_lds_dwordx4 v[54:55], off
	s_waitcnt vmcnt(8)
	s_waitcnt lgkmcnt(0)
	s_barrier
	s_setprio 1
	s_waitcnt lgkmcnt(0)
	.p2align	4
	v_mfma_scale_f32_16x16x128_f8f6f4 v[94:97], v[2:9], v[10:17], v[94:97], v195, v195 op_sel_hi:[0,0,0]
	v_mfma_scale_f32_16x16x128_f8f6f4 v[90:93], v[98:105], v[10:17], v[90:93], v195, v195 op_sel_hi:[0,0,0]
	v_mfma_scale_f32_16x16x128_f8f6f4 v[86:89], v[2:9], v[18:25], v[86:89], v195, v195 op_sel_hi:[0,0,0]
	v_mfma_scale_f32_16x16x128_f8f6f4 v[82:85], v[98:105], v[18:25], v[82:85], v195, v195 op_sel_hi:[0,0,0]
	v_mfma_scale_f32_16x16x128_f8f6f4 v[78:81], v[2:9], v[26:33], v[78:81], v195, v195 op_sel_hi:[0,0,0]
	v_mfma_scale_f32_16x16x128_f8f6f4 v[74:77], v[98:105], v[26:33], v[204:207], v195, v195 op_sel_hi:[0,0,0]
	v_mfma_scale_f32_16x16x128_f8f6f4 v[70:73], v[2:9], v[106:113], v[208:211], v195, v195 op_sel_hi:[0,0,0]
	v_mfma_scale_f32_16x16x128_f8f6f4 v[66:69], v[98:105], v[106:113], v[212:215], v195, v195 op_sel_hi:[0,0,0]
	s_setprio 0
	s_setprio 1
	.p2align	4
	v_mfma_scale_f32_16x16x128_f8f6f4 v[62:65], v[122:129], v[10:17], v[216:219], v195, v195 op_sel_hi:[0,0,0]
	v_mfma_scale_f32_16x16x128_f8f6f4 v[58:61], v[130:137], v[10:17], v[162:165], v195, v195 op_sel_hi:[0,0,0]
	v_mfma_scale_f32_16x16x128_f8f6f4 v[54:57], v[122:129], v[18:25], v[166:169], v195, v195 op_sel_hi:[0,0,0]
	v_mfma_scale_f32_16x16x128_f8f6f4 v[14:17], v[130:137], v[18:25], v[170:173], v195, v195 op_sel_hi:[0,0,0]
	v_mfma_scale_f32_16x16x128_f8f6f4 v[10:13], v[122:129], v[26:33], v[174:177], v195, v195 op_sel_hi:[0,0,0]
	v_mfma_scale_f32_16x16x128_f8f6f4 v[38:41], v[130:137], v[26:33], v[38:41], v195, v195 op_sel_hi:[0,0,0]
	v_mfma_scale_f32_16x16x128_f8f6f4 v[30:33], v[122:129], v[106:113], v[178:181], v195, v195 op_sel_hi:[0,0,0]
	v_mfma_scale_f32_16x16x128_f8f6f4 v[22:25], v[130:137], v[106:113], v[182:185], v195, v195 op_sel_hi:[0,0,0]
	s_setprio 0
	s_barrier
	s_add_i32 s34, s34, s43
	v_add_u32_e32 v18, s85, v1
	ds_read_b128 v[106:109], v18 offset:49152
	ds_read_b128 v[110:113], v18 offset:50176
	ds_read_b128 v[114:117], v18 offset:51200
	ds_read_b128 v[118:121], v18 offset:52224
	ds_read_b128 v[138:141], v18 offset:53248
	ds_read_b128 v[142:145], v18 offset:54272
	ds_read_b128 v[146:149], v18 offset:55296
	ds_read_b128 v[150:153], v18 offset:56320
	s_mov_b32 m0, s34
	v_lshl_add_u64 v[18:19], s[62:63], 0, v[202:203]
	v_lshl_add_u64 v[20:21], v[18:19], 0, s[24:25]
	global_load_lds_dwordx4 v[20:21], off
	v_lshl_add_u64 v[18:19], v[18:19], 0, s[26:27]
	s_add_i32 m0, s34, 0x2000
	s_add_i32 s34, s35, s43
	global_load_lds_dwordx4 v[18:19], off
	s_mov_b32 m0, s34
	v_lshl_add_u64 v[18:19], s[62:63], 0, v[202:203]
	v_lshl_add_u64 v[20:21], v[18:19], 0, s[28:29]
	global_load_lds_dwordx4 v[20:21], off
	v_lshl_add_u64 v[18:19], v[18:19], 0, s[30:31]
	s_add_i32 m0, s34, 0x2000
	s_nop 0
	global_load_lds_dwordx4 v[18:19], off
	s_mov_b32 m0, s82
	v_lshl_add_u64 v[18:19], s[60:61], 0, v[196:197]
	v_lshl_add_u64 v[20:21], v[18:19], 0, s[24:25]
	global_load_lds_dwordx4 v[20:21], off
	v_lshl_add_u64 v[18:19], v[18:19], 0, s[26:27]
	s_mov_b32 m0, s83
	s_nop 0
	global_load_lds_dwordx4 v[18:19], off
	s_waitcnt vmcnt(8)
	s_waitcnt lgkmcnt(0)
	s_barrier
	s_setprio 1
	s_waitcnt lgkmcnt(0)
	.p2align	4
	v_mfma_scale_f32_16x16x128_f8f6f4 v[42:45], v[2:9], v[106:113], v[42:45], v195, v195 op_sel_hi:[0,0,0]
	v_mfma_scale_f32_16x16x128_f8f6f4 v[34:37], v[98:105], v[106:113], v[34:37], v195, v195 op_sel_hi:[0,0,0]
	v_mfma_scale_f32_16x16x128_f8f6f4 v[26:29], v[2:9], v[114:121], v[186:189], v195, v195 op_sel_hi:[0,0,0]
	v_mfma_scale_f32_16x16x128_f8f6f4 v[18:21], v[98:105], v[114:121], v[190:193], v195, v195 op_sel_hi:[0,0,0]
	v_mfma_scale_f32_16x16x128_f8f6f4 v[224:227], v[2:9], v[138:145], v[224:227], v195, v195 op_sel_hi:[0,0,0]
	v_mfma_scale_f32_16x16x128_f8f6f4 v[228:231], v[98:105], v[138:145], v[228:231], v195, v195 op_sel_hi:[0,0,0]
	v_mfma_scale_f32_16x16x128_f8f6f4 v[6:9], v[2:9], v[146:153], v[232:235], v195, v195 op_sel_hi:[0,0,0]
	v_mfma_scale_f32_16x16x128_f8f6f4 v[2:5], v[98:105], v[146:153], v[236:239], v195, v195 op_sel_hi:[0,0,0]
	s_setprio 0
	s_setprio 1
	.p2align	4
	v_mfma_scale_f32_16x16x128_f8f6f4 v[98:101], v[122:129], v[106:113], v[240:243], v195, v195 op_sel_hi:[0,0,0]
	v_mfma_scale_f32_16x16x128_f8f6f4 v[102:105], v[130:137], v[106:113], v[244:247], v195, v195 op_sel_hi:[0,0,0]
	v_mfma_scale_f32_16x16x128_f8f6f4 v[106:109], v[122:129], v[114:121], v[248:251], v195, v195 op_sel_hi:[0,0,0]
	v_mfma_scale_f32_16x16x128_f8f6f4 v[110:113], v[130:137], v[114:121], v[198:201], v195, v195 op_sel_hi:[0,0,0]
	v_mfma_scale_f32_16x16x128_f8f6f4 v[114:117], v[122:129], v[138:145], v[220:223], v195, v195 op_sel_hi:[0,0,0]
	v_mfma_scale_f32_16x16x128_f8f6f4 v[118:121], v[130:137], v[138:145], v[46:49], v195, v195 op_sel_hi:[0,0,0]
	v_mfma_scale_f32_16x16x128_f8f6f4 v[122:125], v[122:129], v[146:153], v[50:53], v195, v195 op_sel_hi:[0,0,0]
	v_mfma_scale_f32_16x16x128_f8f6f4 v[126:129], v[130:137], v[146:153], v[154:157], v195, v195 op_sel_hi:[0,0,0]
	s_setprio 0
	s_barrier
	s_add_i32 s70, s70, 2
	s_add_u32 s58, s58, 0x100
	s_addc_u32 s59, s59, 0
	s_add_u32 s68, s68, 0x100
	s_addc_u32 s69, s69, 0
	s_cmp_gt_u32 s70, 5
	s_cbranch_scc0 .LBB0_977
	s_and_b64 vcc, exec, s[36:37]
	s_cbranch_vccz .LBB0_980
	s_barrier

.LBB0_1074:
	s_add_u32 s2, s54, 0xfffa0080
	v_add_u32_e32 v146, s66, v1
	v_add_u32_e32 v142, s71, v146
	v_add_u32_e32 v154, s72, v146
	ds_read_b128 v[130:133], v142
	ds_read_b128 v[134:137], v142 offset:1024
	ds_read_b128 v[138:141], v142 offset:2048
	ds_read_b128 v[142:145], v142 offset:3072
	ds_read_b128 v[146:149], v154
	ds_read_b128 v[150:153], v154 offset:1024
	ds_read_b128 v[172:175], v154 offset:2048
	ds_read_b128 v[176:179], v154 offset:3072
	s_addc_u32 s34, s55, -1
	s_cmp_eq_u32 s76, 12
	s_cselect_b32 s57, s38, s34
	s_cselect_b32 s56, s39, s2
	s_cselect_b32 s59, s41, s75
	s_cselect_b32 s58, s43, s74
	v_add_u32_e32 v154, s67, v1
	s_mov_b32 s34, 0xfffe0000
	ds_read_b128 v[180:183], v154
	ds_read_b128 v[184:187], v154 offset:1024
	ds_read_b128 v[196:199], v154 offset:2048
	ds_read_b128 v[200:203], v154 offset:3072
	ds_read_b128 v[204:207], v154 offset:4096
	ds_read_b128 v[208:211], v154 offset:5120
	ds_read_b128 v[212:215], v154 offset:6144
	ds_read_b128 v[216:219], v154 offset:7168
	s_mov_b32 s35, -1
	v_lshl_add_u64 v[154:155], s[54:55], 0, v[158:159]
	v_lshl_add_u64 v[154:155], v[154:155], 0, s[34:35]
	s_add_i32 m0, s51, 0xc000
	s_nop 0
	global_load_lds_dwordx4 v[154:155], off
	s_add_i32 m0, s51, 0xe000
	s_nop 0
	global_load_lds_dwordx4 v158, s[54:55]
	s_waitcnt vmcnt(8)
	s_waitcnt lgkmcnt(0)
	s_barrier
	s_setprio 1
	s_waitcnt lgkmcnt(0)
	.p2align	4
	v_mfma_scale_f32_16x16x128_f8f6f4 v[126:129], v[130:137], v[180:187], v[126:129], v170, v170 op_sel_hi:[0,0,0]
	v_mfma_scale_f32_16x16x128_f8f6f4 v[122:125], v[138:145], v[180:187], v[122:125], v170, v170 op_sel_hi:[0,0,0]
	v_mfma_scale_f32_16x16x128_f8f6f4 v[114:117], v[130:137], v[196:203], v[114:117], v170, v170 op_sel_hi:[0,0,0]
	v_mfma_scale_f32_16x16x128_f8f6f4 v[106:109], v[138:145], v[196:203], v[106:109], v170, v170 op_sel_hi:[0,0,0]
	v_mfma_scale_f32_16x16x128_f8f6f4 v[98:101], v[130:137], v[204:211], v[98:101], v170, v170 op_sel_hi:[0,0,0]
	v_mfma_scale_f32_16x16x128_f8f6f4 v[154:157], v[138:145], v[204:211], v[90:93], v170, v170 op_sel_hi:[0,0,0]
	v_mfma_scale_f32_16x16x128_f8f6f4 v[166:169], v[130:137], v[212:219], v[82:85], v170, v170 op_sel_hi:[0,0,0]
	v_mfma_scale_f32_16x16x128_f8f6f4 v[188:191], v[138:145], v[212:219], v[74:77], v170, v170 op_sel_hi:[0,0,0]
	s_setprio 0
	s_setprio 1
	.p2align	4
	v_mfma_scale_f32_16x16x128_f8f6f4 v[118:121], v[146:153], v[180:187], v[118:121], v170, v170 op_sel_hi:[0,0,0]
	v_mfma_scale_f32_16x16x128_f8f6f4 v[110:113], v[172:179], v[180:187], v[110:113], v170, v170 op_sel_hi:[0,0,0]
	v_mfma_scale_f32_16x16x128_f8f6f4 v[102:105], v[146:153], v[196:203], v[102:105], v170, v170 op_sel_hi:[0,0,0]
	v_mfma_scale_f32_16x16x128_f8f6f4 v[180:183], v[172:179], v[196:203], v[94:97], v170, v170 op_sel_hi:[0,0,0]
	v_mfma_scale_f32_16x16x128_f8f6f4 v[184:187], v[146:153], v[204:211], v[86:89], v170, v170 op_sel_hi:[0,0,0]
	v_mfma_scale_f32_16x16x128_f8f6f4 v[192:195], v[172:179], v[204:211], v[78:81], v170, v170 op_sel_hi:[0,0,0]
	v_mfma_scale_f32_16x16x128_f8f6f4 v[196:199], v[146:153], v[212:219], v[70:73], v170, v170 op_sel_hi:[0,0,0]
	v_mfma_scale_f32_16x16x128_f8f6f4 v[200:203], v[172:179], v[212:219], v[66:69], v170, v170 op_sel_hi:[0,0,0]
	s_setprio 0
	s_barrier
	v_mov_b32_e32 v165, v159
	v_add_u32_e32 v94, s67, v1
	s_add_i32 s2, s71, s37
	s_nop 1
	ds_read_b128 v[66:69], v94 offset:16384
	ds_read_b128 v[70:73], v94 offset:17408
	ds_read_b128 v[74:77], v94 offset:18432
	ds_read_b128 v[78:81], v94 offset:19456
	ds_read_b128 v[82:85], v94 offset:20480
	ds_read_b128 v[86:89], v94 offset:21504
	ds_read_b128 v[90:93], v94 offset:22528
	ds_read_b128 v[94:97], v94 offset:23552
	s_mov_b32 m0, s2
	v_lshl_add_u64 v[204:205], s[58:59], 0, v[164:165]
	global_load_lds_dwordx4 v164, s[58:59]
	v_lshl_add_u64 v[204:205], v[204:205], 0, s[12:13]
	s_add_i32 m0, s2, 0x2000
	s_add_i32 s2, s72, s37
	global_load_lds_dwordx4 v[204:205], off
	s_mov_b32 m0, s2
	v_lshl_add_u64 v[204:205], s[58:59], 0, v[164:165]
	v_lshl_add_u64 v[206:207], v[204:205], 0, s[14:15]
	global_load_lds_dwordx4 v[206:207], off
	v_lshl_add_u64 v[204:205], v[204:205], 0, s[16:17]
	s_add_i32 m0, s2, 0x2000
	s_nop 0
	global_load_lds_dwordx4 v[204:205], off
	s_mov_b32 m0, s51
	v_lshl_add_u64 v[204:205], s[56:57], 0, v[158:159]
	global_load_lds_dwordx4 v158, s[56:57]
	v_lshl_add_u64 v[204:205], v[204:205], 0, s[12:13]
	s_mov_b32 m0, s60
	s_nop 0
	global_load_lds_dwordx4 v[204:205], off
	s_waitcnt vmcnt(8)
	s_waitcnt lgkmcnt(0)
	s_barrier
	s_setprio 1
	s_waitcnt lgkmcnt(0)
	.p2align	4
	v_mfma_scale_f32_16x16x128_f8f6f4 v[54:57], v[130:137], v[66:73], v[54:57], v170, v170 op_sel_hi:[0,0,0]
	v_mfma_scale_f32_16x16x128_f8f6f4 v[18:21], v[130:137], v[82:89], v[18:21], v170, v170 op_sel_hi:[0,0,0]
	v_mfma_scale_f32_16x16x128_f8f6f4 v[204:207], v[138:145], v[66:73], v[50:53], v170, v170 op_sel_hi:[0,0,0]
	v_mfma_scale_f32_16x16x128_f8f6f4 v[208:211], v[130:137], v[74:81], v[38:41], v170, v170 op_sel_hi:[0,0,0]
	v_mfma_scale_f32_16x16x128_f8f6f4 v[212:215], v[138:145], v[74:81], v[30:33], v170, v170 op_sel_hi:[0,0,0]
	v_mfma_scale_f32_16x16x128_f8f6f4 v[216:219], v[138:145], v[82:89], v[10:13], v170, v170 op_sel_hi:[0,0,0]
	v_mfma_scale_f32_16x16x128_f8f6f4 v[220:223], v[130:137], v[90:97], v[6:9], v170, v170 op_sel_hi:[0,0,0]
	v_mfma_scale_f32_16x16x128_f8f6f4 v[224:227], v[138:145], v[90:97], v[2:5], v170, v170 op_sel_hi:[0,0,0]
	s_setprio 0
	s_setprio 1
	.p2align	4
	v_mfma_scale_f32_16x16x128_f8f6f4 v[62:65], v[146:153], v[66:73], v[62:65], v170, v170 op_sel_hi:[0,0,0]
	v_mfma_scale_f32_16x16x128_f8f6f4 v[58:61], v[172:179], v[66:73], v[58:61], v170, v170 op_sel_hi:[0,0,0]
	v_mfma_scale_f32_16x16x128_f8f6f4 v[228:231], v[146:153], v[74:81], v[46:49], v170, v170 op_sel_hi:[0,0,0]
	v_mfma_scale_f32_16x16x128_f8f6f4 v[232:235], v[172:179], v[74:81], v[42:45], v170, v170 op_sel_hi:[0,0,0]
	v_mfma_scale_f32_16x16x128_f8f6f4 v[236:239], v[146:153], v[82:89], v[34:37], v170, v170 op_sel_hi:[0,0,0]
	v_mfma_scale_f32_16x16x128_f8f6f4 v[240:243], v[172:179], v[82:89], v[26:29], v170, v170 op_sel_hi:[0,0,0]
	v_mfma_scale_f32_16x16x128_f8f6f4 v[244:247], v[146:153], v[90:97], v[22:25], v170, v170 op_sel_hi:[0,0,0]
	v_mfma_scale_f32_16x16x128_f8f6f4 v[248:251], v[172:179], v[90:97], v[14:17], v170, v170 op_sel_hi:[0,0,0]
	s_setprio 0
	s_barrier
	s_add_i32 s2, 0, 0x18000
	v_add_u32_e32 v10, s66, v1
	s_add_i32 s34, 0, 0x1c000
	v_add_u32_e32 v11, s2, v10
	v_add_u32_e32 v10, s34, v10
	ds_read_b128 v[2:5], v11
	ds_read_b128 v[6:9], v11 offset:1024
	ds_read_b128 v[22:25], v11 offset:2048
	ds_read_b128 v[26:29], v11 offset:3072
	ds_read_b128 v[130:133], v10
	ds_read_b128 v[134:137], v10 offset:1024
	ds_read_b128 v[138:141], v10 offset:2048
	ds_read_b128 v[142:145], v10 offset:3072
	v_add_u32_e32 v50, s67, v1
	ds_read_b128 v[10:13], v50 offset:32768
	ds_read_b128 v[14:17], v50 offset:33792
	ds_read_b128 v[30:33], v50 offset:34816
	ds_read_b128 v[34:37], v50 offset:35840
	ds_read_b128 v[38:41], v50 offset:36864
	ds_read_b128 v[42:45], v50 offset:37888
	ds_read_b128 v[46:49], v50 offset:38912
	ds_read_b128 v[50:53], v50 offset:39936
	s_mov_b32 m0, s61
	v_lshl_add_u64 v[66:67], s[56:57], 0, v[158:159]
	v_lshl_add_u64 v[68:69], v[66:67], 0, s[14:15]
	global_load_lds_dwordx4 v[68:69], off
	v_lshl_add_u64 v[66:67], v[66:67], 0, s[16:17]
	s_mov_b32 m0, s62
	s_nop 0
	global_load_lds_dwordx4 v[66:67], off
	s_waitcnt vmcnt(8)
	s_waitcnt lgkmcnt(0)
	s_barrier
	s_setprio 1
	s_waitcnt lgkmcnt(0)
	.p2align	4
	v_mfma_scale_f32_16x16x128_f8f6f4 v[126:129], v[2:9], v[10:17], v[126:129], v170, v170 op_sel_hi:[0,0,0]
	v_mfma_scale_f32_16x16x128_f8f6f4 v[122:125], v[22:29], v[10:17], v[122:125], v170, v170 op_sel_hi:[0,0,0]
	v_mfma_scale_f32_16x16x128_f8f6f4 v[114:117], v[2:9], v[30:37], v[114:117], v170, v170 op_sel_hi:[0,0,0]
	v_mfma_scale_f32_16x16x128_f8f6f4 v[106:109], v[22:29], v[30:37], v[106:109], v170, v170 op_sel_hi:[0,0,0]
	v_mfma_scale_f32_16x16x128_f8f6f4 v[98:101], v[2:9], v[38:45], v[98:101], v170, v170 op_sel_hi:[0,0,0]
	v_mfma_scale_f32_16x16x128_f8f6f4 v[90:93], v[22:29], v[38:45], v[154:157], v170, v170 op_sel_hi:[0,0,0]
	v_mfma_scale_f32_16x16x128_f8f6f4 v[82:85], v[2:9], v[46:53], v[166:169], v170, v170 op_sel_hi:[0,0,0]
	v_mfma_scale_f32_16x16x128_f8f6f4 v[74:77], v[22:29], v[46:53], v[188:191], v170, v170 op_sel_hi:[0,0,0]
	s_setprio 0
	s_setprio 1
	.p2align	4
	v_mfma_scale_f32_16x16x128_f8f6f4 v[118:121], v[130:137], v[10:17], v[118:121], v170, v170 op_sel_hi:[0,0,0]
	v_mfma_scale_f32_16x16x128_f8f6f4 v[110:113], v[138:145], v[10:17], v[110:113], v170, v170 op_sel_hi:[0,0,0]
	v_mfma_scale_f32_16x16x128_f8f6f4 v[102:105], v[130:137], v[30:37], v[102:105], v170, v170 op_sel_hi:[0,0,0]
	v_mfma_scale_f32_16x16x128_f8f6f4 v[94:97], v[138:145], v[30:37], v[180:183], v170, v170 op_sel_hi:[0,0,0]
	v_mfma_scale_f32_16x16x128_f8f6f4 v[86:89], v[130:137], v[38:45], v[184:187], v170, v170 op_sel_hi:[0,0,0]
	v_mfma_scale_f32_16x16x128_f8f6f4 v[78:81], v[138:145], v[38:45], v[192:195], v170, v170 op_sel_hi:[0,0,0]
	v_mfma_scale_f32_16x16x128_f8f6f4 v[70:73], v[130:137], v[46:53], v[196:199], v170, v170 op_sel_hi:[0,0,0]
	v_mfma_scale_f32_16x16x128_f8f6f4 v[66:69], v[138:145], v[46:53], v[200:203], v170, v170 op_sel_hi:[0,0,0]
	s_setprio 0
	s_barrier
	s_add_i32 s2, s2, s37
	v_add_u32_e32 v10, s67, v1
	ds_read_b128 v[42:45], v10 offset:49152
	ds_read_b128 v[46:49], v10 offset:50176
	ds_read_b128 v[146:149], v10 offset:51200
	ds_read_b128 v[150:153], v10 offset:52224
	ds_read_b128 v[172:175], v10 offset:53248
	ds_read_b128 v[176:179], v10 offset:54272
	ds_read_b128 v[180:183], v10 offset:55296
	ds_read_b128 v[184:187], v10 offset:56320
	s_mov_b32 m0, s2
	v_lshl_add_u64 v[10:11], s[58:59], 0, v[164:165]
	v_lshl_add_u64 v[12:13], v[10:11], 0, s[22:23]
	global_load_lds_dwordx4 v[12:13], off
	v_lshl_add_u64 v[10:11], v[10:11], 0, s[24:25]
	s_add_i32 m0, s2, 0x2000
	s_add_i32 s2, s34, s37
	global_load_lds_dwordx4 v[10:11], off
	s_mov_b32 m0, s2
	v_lshl_add_u64 v[10:11], s[58:59], 0, v[164:165]
	v_lshl_add_u64 v[12:13], v[10:11], 0, s[26:27]
	global_load_lds_dwordx4 v[12:13], off
	v_lshl_add_u64 v[10:11], v[10:11], 0, s[28:29]
	s_add_i32 m0, s2, 0x2000
	s_nop 0
	global_load_lds_dwordx4 v[10:11], off
	s_mov_b32 m0, s64
	v_lshl_add_u64 v[10:11], s[56:57], 0, v[158:159]
	v_lshl_add_u64 v[12:13], v[10:11], 0, s[22:23]
	global_load_lds_dwordx4 v[12:13], off
	v_lshl_add_u64 v[10:11], v[10:11], 0, s[24:25]
	s_mov_b32 m0, s65
	s_nop 0
	global_load_lds_dwordx4 v[10:11], off
	s_waitcnt vmcnt(8)
	s_waitcnt lgkmcnt(0)
	s_barrier
	s_setprio 1
	s_waitcnt lgkmcnt(0)
	.p2align	4
	v_mfma_scale_f32_16x16x128_f8f6f4 v[54:57], v[2:9], v[42:49], v[54:57], v170, v170 op_sel_hi:[0,0,0]
	v_mfma_scale_f32_16x16x128_f8f6f4 v[50:53], v[22:29], v[42:49], v[204:207], v170, v170 op_sel_hi:[0,0,0]
	v_mfma_scale_f32_16x16x128_f8f6f4 v[38:41], v[2:9], v[146:153], v[208:211], v170, v170 op_sel_hi:[0,0,0]
	v_mfma_scale_f32_16x16x128_f8f6f4 v[30:33], v[22:29], v[146:153], v[212:215], v170, v170 op_sel_hi:[0,0,0]
	v_mfma_scale_f32_16x16x128_f8f6f4 v[18:21], v[2:9], v[172:179], v[18:21], v170, v170 op_sel_hi:[0,0,0]
	v_mfma_scale_f32_16x16x128_f8f6f4 v[10:13], v[22:29], v[172:179], v[216:219], v170, v170 op_sel_hi:[0,0,0]
	v_mfma_scale_f32_16x16x128_f8f6f4 v[6:9], v[2:9], v[180:187], v[220:223], v170, v170 op_sel_hi:[0,0,0]
	v_mfma_scale_f32_16x16x128_f8f6f4 v[2:5], v[22:29], v[180:187], v[224:227], v170, v170 op_sel_hi:[0,0,0]
	s_setprio 0
	s_setprio 1
	.p2align	4
	v_mfma_scale_f32_16x16x128_f8f6f4 v[62:65], v[130:137], v[42:49], v[62:65], v170, v170 op_sel_hi:[0,0,0]
	v_mfma_scale_f32_16x16x128_f8f6f4 v[58:61], v[138:145], v[42:49], v[58:61], v170, v170 op_sel_hi:[0,0,0]
	v_mfma_scale_f32_16x16x128_f8f6f4 v[46:49], v[130:137], v[146:153], v[228:231], v170, v170 op_sel_hi:[0,0,0]
	v_mfma_scale_f32_16x16x128_f8f6f4 v[42:45], v[138:145], v[146:153], v[232:235], v170, v170 op_sel_hi:[0,0,0]
	v_mfma_scale_f32_16x16x128_f8f6f4 v[34:37], v[130:137], v[172:179], v[236:239], v170, v170 op_sel_hi:[0,0,0]
	v_mfma_scale_f32_16x16x128_f8f6f4 v[26:29], v[138:145], v[172:179], v[240:243], v170, v170 op_sel_hi:[0,0,0]
	v_mfma_scale_f32_16x16x128_f8f6f4 v[22:25], v[130:137], v[180:187], v[244:247], v170, v170 op_sel_hi:[0,0,0]
	v_mfma_scale_f32_16x16x128_f8f6f4 v[14:17], v[138:145], v[180:187], v[248:251], v170, v170 op_sel_hi:[0,0,0]
	s_setprio 0
	s_barrier
	s_add_i32 s76, s76, 2
	s_add_u32 s54, s54, 0x100
	s_addc_u32 s55, s55, 0
	s_add_u32 s74, s74, 0x100
	s_addc_u32 s75, s75, 0
	s_cmp_gt_u32 s76, 13
	s_cbranch_scc0 .LBB0_1074
	s_and_b64 vcc, exec, s[30:31]
	s_cbranch_vccz .LBB0_1077
	s_barrier

.LBB0_1224:
	s_add_u32 s64, s46, s58
	v_add_u32_e32 v42, s76, v1
	v_add_u32_e32 v43, s79, v42
	v_add_u32_e32 v42, s81, v42
	ds_read_b128 v[140:143], v43
	ds_read_b128 v[144:147], v43 offset:1024
	ds_read_b128 v[148:151], v43 offset:2048
	ds_read_b128 v[152:155], v43 offset:3072
	ds_read_b128 v[156:159], v42
	ds_read_b128 v[160:163], v42 offset:1024
	ds_read_b128 v[164:167], v42 offset:2048
	ds_read_b128 v[168:171], v42 offset:3072
	s_addc_u32 s65, s47, s59
	s_add_u32 s34, s64, 0x100
	s_addc_u32 s35, s65, 0
	s_add_u32 s62, s2, s58
	s_addc_u32 s63, s49, s59
	s_cmpk_eq_i32 s58, 0x700
	s_cselect_b32 s61, s55, s35
	s_cselect_b32 s60, s54, s34
	s_cselect_b32 s63, s57, s63
	s_cselect_b32 s62, s56, s62
	v_add_u32_e32 v42, s77, v1
	v_mov_b64_e32 v[46:47], v[172:173]
	v_mov_b64_e32 v[50:51], v[176:177]
	v_mov_b64_e32 v[48:49], v[174:175]
	ds_read_b128 v[172:175], v42
	v_mov_b64_e32 v[52:53], v[178:179]
	ds_read_b128 v[176:179], v42 offset:1024
	ds_read_b128 v[180:183], v42 offset:2048
	ds_read_b128 v[184:187], v42 offset:3072
	ds_read_b128 v[196:199], v42 offset:4096
	ds_read_b128 v[200:203], v42 offset:5120
	ds_read_b128 v[204:207], v42 offset:6144
	ds_read_b128 v[208:211], v42 offset:7168
	s_add_i32 m0, s27, 0xc000
	v_lshl_add_u64 v[42:43], s[64:65], 0, v[130:131]
	v_lshl_add_u64 v[44:45], v[42:43], 0, s[38:39]
	global_load_lds_dwordx4 v[44:45], off
	v_lshl_add_u64 v[42:43], v[42:43], 0, s[40:41]
	s_add_i32 m0, s27, 0xe000
	s_nop 0
	global_load_lds_dwordx4 v[42:43], off
	s_waitcnt vmcnt(8)
	s_waitcnt lgkmcnt(0)
	s_barrier
	s_setprio 1
	s_waitcnt lgkmcnt(0)
	.p2align	4
	v_mfma_scale_f32_16x16x128_f8f6f4 v[94:97], v[140:147], v[172:179], v[94:97], v138, v138 op_sel_hi:[0,0,0]
	v_mfma_scale_f32_16x16x128_f8f6f4 v[90:93], v[148:155], v[172:179], v[90:93], v138, v138 op_sel_hi:[0,0,0]
	v_mfma_scale_f32_16x16x128_f8f6f4 v[86:89], v[140:147], v[180:187], v[86:89], v138, v138 op_sel_hi:[0,0,0]
	v_mfma_scale_f32_16x16x128_f8f6f4 v[82:85], v[148:155], v[180:187], v[82:85], v138, v138 op_sel_hi:[0,0,0]
	v_mfma_scale_f32_16x16x128_f8f6f4 v[78:81], v[140:147], v[196:203], v[78:81], v138, v138 op_sel_hi:[0,0,0]
	v_mfma_scale_f32_16x16x128_f8f6f4 v[74:77], v[148:155], v[196:203], v[74:77], v138, v138 op_sel_hi:[0,0,0]
	v_mfma_scale_f32_16x16x128_f8f6f4 v[134:137], v[140:147], v[204:211], v[70:73], v138, v138 op_sel_hi:[0,0,0]
	v_mfma_scale_f32_16x16x128_f8f6f4 v[188:191], v[148:155], v[204:211], v[66:69], v138, v138 op_sel_hi:[0,0,0]
	s_setprio 0
	s_setprio 1
	.p2align	4
	v_mfma_scale_f32_16x16x128_f8f6f4 v[192:195], v[156:163], v[172:179], v[62:65], v138, v138 op_sel_hi:[0,0,0]
	v_mfma_scale_f32_16x16x128_f8f6f4 v[172:175], v[164:171], v[172:179], v[58:61], v138, v138 op_sel_hi:[0,0,0]
	v_mfma_scale_f32_16x16x128_f8f6f4 v[176:179], v[156:163], v[180:187], v[54:57], v138, v138 op_sel_hi:[0,0,0]
	v_mfma_scale_f32_16x16x128_f8f6f4 v[180:183], v[164:171], v[180:187], v[50:53], v138, v138 op_sel_hi:[0,0,0]
	v_mfma_scale_f32_16x16x128_f8f6f4 v[184:187], v[156:163], v[196:203], v[46:49], v138, v138 op_sel_hi:[0,0,0]
	v_mfma_scale_f32_16x16x128_f8f6f4 v[196:199], v[164:171], v[196:203], v[18:21], v138, v138 op_sel_hi:[0,0,0]
	v_mfma_scale_f32_16x16x128_f8f6f4 v[200:203], v[156:163], v[204:211], v[6:9], v138, v138 op_sel_hi:[0,0,0]
	v_mfma_scale_f32_16x16x128_f8f6f4 v[204:207], v[164:171], v[204:211], v[14:17], v138, v138 op_sel_hi:[0,0,0]
	s_setprio 0
	s_barrier
	v_mov_b32_e32 v133, v131
	s_nop 2
	v_add_u32_e32 v6, s77, v1
	s_add_i32 s34, s79, s3
	ds_read_b128 v[42:45], v6 offset:16384
	ds_read_b128 v[46:49], v6 offset:17408
	ds_read_b128 v[50:53], v6 offset:18432
	ds_read_b128 v[54:57], v6 offset:19456
	ds_read_b128 v[58:61], v6 offset:20480
	ds_read_b128 v[62:65], v6 offset:21504
	ds_read_b128 v[66:69], v6 offset:22528
	ds_read_b128 v[70:73], v6 offset:23552
	s_mov_b32 m0, s34
	v_lshl_add_u64 v[6:7], s[62:63], 0, v[132:133]
	global_load_lds_dwordx4 v132, s[62:63]
	v_lshl_add_u64 v[6:7], v[6:7], 0, s[20:21]
	s_add_i32 m0, s34, 0x2000
	s_add_i32 s34, s81, s3
	global_load_lds_dwordx4 v[6:7], off
	s_mov_b32 m0, s34
	v_lshl_add_u64 v[6:7], s[62:63], 0, v[132:133]
	v_lshl_add_u64 v[8:9], v[6:7], 0, s[22:23]
	global_load_lds_dwordx4 v[8:9], off
	v_lshl_add_u64 v[6:7], v[6:7], 0, s[24:25]
	s_add_i32 m0, s34, 0x2000
	s_nop 0
	global_load_lds_dwordx4 v[6:7], off
	s_mov_b32 m0, s27
	v_lshl_add_u64 v[6:7], s[60:61], 0, v[130:131]
	global_load_lds_dwordx4 v130, s[60:61]
	v_lshl_add_u64 v[6:7], v[6:7], 0, s[20:21]
	s_mov_b32 m0, s70
	s_nop 0
	global_load_lds_dwordx4 v[6:7], off
	s_waitcnt vmcnt(8)
	s_waitcnt lgkmcnt(0)
	s_barrier
	s_setprio 1
	s_waitcnt lgkmcnt(0)
	.p2align	4
	v_mfma_scale_f32_16x16x128_f8f6f4 v[38:41], v[140:147], v[42:49], v[38:41], v138, v138 op_sel_hi:[0,0,0]
	v_mfma_scale_f32_16x16x128_f8f6f4 v[34:37], v[148:155], v[42:49], v[34:37], v138, v138 op_sel_hi:[0,0,0]
	v_mfma_scale_f32_16x16x128_f8f6f4 v[220:223], v[148:155], v[58:65], v[220:223], v138, v138 op_sel_hi:[0,0,0]
	v_mfma_scale_f32_16x16x128_f8f6f4 v[208:211], v[140:147], v[50:57], v[30:33], v138, v138 op_sel_hi:[0,0,0]
	v_mfma_scale_f32_16x16x128_f8f6f4 v[212:215], v[148:155], v[50:57], v[26:29], v138, v138 op_sel_hi:[0,0,0]
	v_mfma_scale_f32_16x16x128_f8f6f4 v[216:219], v[140:147], v[58:65], v[22:25], v138, v138 op_sel_hi:[0,0,0]
	v_mfma_scale_f32_16x16x128_f8f6f4 v[224:227], v[140:147], v[66:73], v[2:5], v138, v138 op_sel_hi:[0,0,0]
	v_mfma_scale_f32_16x16x128_f8f6f4 v[228:231], v[148:155], v[66:73], v[10:13], v138, v138 op_sel_hi:[0,0,0]
	s_setprio 0
	s_setprio 1
	.p2align	4
	v_mfma_scale_f32_16x16x128_f8f6f4 v[232:235], v[156:163], v[42:49], v[98:101], v138, v138 op_sel_hi:[0,0,0]
	v_mfma_scale_f32_16x16x128_f8f6f4 v[236:239], v[164:171], v[42:49], v[102:105], v138, v138 op_sel_hi:[0,0,0]
	v_mfma_scale_f32_16x16x128_f8f6f4 v[240:243], v[156:163], v[50:57], v[106:109], v138, v138 op_sel_hi:[0,0,0]
	v_mfma_scale_f32_16x16x128_f8f6f4 v[244:247], v[164:171], v[50:57], v[110:113], v138, v138 op_sel_hi:[0,0,0]
	v_mfma_scale_f32_16x16x128_f8f6f4 v[248:251], v[156:163], v[58:65], v[114:117], v138, v138 op_sel_hi:[0,0,0]
	v_mfma_scale_f32_16x16x128_f8f6f4 v[42:45], v[164:171], v[58:65], v[118:121], v138, v138 op_sel_hi:[0,0,0]
	v_mfma_scale_f32_16x16x128_f8f6f4 v[46:49], v[156:163], v[66:73], v[122:125], v138, v138 op_sel_hi:[0,0,0]
	v_mfma_scale_f32_16x16x128_f8f6f4 v[50:53], v[164:171], v[66:73], v[126:129], v138, v138 op_sel_hi:[0,0,0]
	s_setprio 0
	s_barrier
	s_add_i32 s34, 0, 0x18000
	v_add_u32_e32 v2, s76, v1
	s_add_i32 s35, 0, 0x1c000
	v_add_u32_e32 v3, s34, v2
	v_add_u32_e32 v2, s35, v2
	ds_read_b128 v[98:101], v3
	ds_read_b128 v[102:105], v3 offset:1024
	ds_read_b128 v[106:109], v3 offset:2048
	ds_read_b128 v[110:113], v3 offset:3072
	ds_read_b128 v[122:125], v2
	ds_read_b128 v[126:129], v2 offset:1024
	ds_read_b128 v[140:143], v2 offset:2048
	ds_read_b128 v[144:147], v2 offset:3072
	v_add_u32_e32 v30, s77, v1
	ds_read_b128 v[2:5], v30 offset:32768
	ds_read_b128 v[6:9], v30 offset:33792
	ds_read_b128 v[10:13], v30 offset:34816
	ds_read_b128 v[14:17], v30 offset:35840
	ds_read_b128 v[18:21], v30 offset:36864
	ds_read_b128 v[22:25], v30 offset:37888
	ds_read_b128 v[26:29], v30 offset:38912
	ds_read_b128 v[30:33], v30 offset:39936
	s_mov_b32 m0, s71
	v_lshl_add_u64 v[54:55], s[60:61], 0, v[130:131]
	v_lshl_add_u64 v[56:57], v[54:55], 0, s[22:23]
	global_load_lds_dwordx4 v[56:57], off
	v_lshl_add_u64 v[54:55], v[54:55], 0, s[24:25]
	s_mov_b32 m0, s72
	s_nop 0
	global_load_lds_dwordx4 v[54:55], off
	s_waitcnt vmcnt(8)
	s_waitcnt lgkmcnt(0)
	s_barrier
	s_setprio 1
	s_waitcnt lgkmcnt(0)
	.p2align	4
	v_mfma_scale_f32_16x16x128_f8f6f4 v[94:97], v[98:105], v[2:9], v[94:97], v138, v138 op_sel_hi:[0,0,0]
	v_mfma_scale_f32_16x16x128_f8f6f4 v[90:93], v[106:113], v[2:9], v[90:93], v138, v138 op_sel_hi:[0,0,0]
	v_mfma_scale_f32_16x16x128_f8f6f4 v[86:89], v[98:105], v[10:17], v[86:89], v138, v138 op_sel_hi:[0,0,0]
	v_mfma_scale_f32_16x16x128_f8f6f4 v[82:85], v[106:113], v[10:17], v[82:85], v138, v138 op_sel_hi:[0,0,0]
	v_mfma_scale_f32_16x16x128_f8f6f4 v[78:81], v[98:105], v[18:25], v[78:81], v138, v138 op_sel_hi:[0,0,0]
	v_mfma_scale_f32_16x16x128_f8f6f4 v[74:77], v[106:113], v[18:25], v[74:77], v138, v138 op_sel_hi:[0,0,0]
	v_mfma_scale_f32_16x16x128_f8f6f4 v[70:73], v[98:105], v[26:33], v[134:137], v138, v138 op_sel_hi:[0,0,0]
	v_mfma_scale_f32_16x16x128_f8f6f4 v[66:69], v[106:113], v[26:33], v[188:191], v138, v138 op_sel_hi:[0,0,0]
	s_setprio 0
	s_setprio 1
	.p2align	4
	v_mfma_scale_f32_16x16x128_f8f6f4 v[62:65], v[122:129], v[2:9], v[192:195], v138, v138 op_sel_hi:[0,0,0]
	v_mfma_scale_f32_16x16x128_f8f6f4 v[58:61], v[140:147], v[2:9], v[172:175], v138, v138 op_sel_hi:[0,0,0]
	v_mfma_scale_f32_16x16x128_f8f6f4 v[54:57], v[122:129], v[10:17], v[176:179], v138, v138 op_sel_hi:[0,0,0]
	v_mfma_scale_f32_16x16x128_f8f6f4 v[176:179], v[140:147], v[10:17], v[180:183], v138, v138 op_sel_hi:[0,0,0]
	v_mfma_scale_f32_16x16x128_f8f6f4 v[172:175], v[122:129], v[18:25], v[184:187], v138, v138 op_sel_hi:[0,0,0]
	v_mfma_scale_f32_16x16x128_f8f6f4 v[18:21], v[140:147], v[18:25], v[196:199], v138, v138 op_sel_hi:[0,0,0]
	v_mfma_scale_f32_16x16x128_f8f6f4 v[6:9], v[122:129], v[26:33], v[200:203], v138, v138 op_sel_hi:[0,0,0]
	v_mfma_scale_f32_16x16x128_f8f6f4 v[14:17], v[140:147], v[26:33], v[204:207], v138, v138 op_sel_hi:[0,0,0]
	s_setprio 0
	s_barrier
	s_add_i32 s34, s34, s3
	v_add_u32_e32 v2, s77, v1
	ds_read_b128 v[114:117], v2 offset:49152
	ds_read_b128 v[118:121], v2 offset:50176
	ds_read_b128 v[148:151], v2 offset:51200
	ds_read_b128 v[152:155], v2 offset:52224
	ds_read_b128 v[156:159], v2 offset:53248
	ds_read_b128 v[160:163], v2 offset:54272
	ds_read_b128 v[164:167], v2 offset:55296
	ds_read_b128 v[168:171], v2 offset:56320
	s_mov_b32 m0, s34
	v_lshl_add_u64 v[2:3], s[62:63], 0, v[132:133]
	v_lshl_add_u64 v[4:5], v[2:3], 0, s[30:31]
	global_load_lds_dwordx4 v[4:5], off
	v_lshl_add_u64 v[2:3], v[2:3], 0, s[36:37]
	s_add_i32 m0, s34, 0x2000
	s_add_i32 s34, s35, s3
	global_load_lds_dwordx4 v[2:3], off
	s_mov_b32 m0, s34
	v_lshl_add_u64 v[2:3], s[62:63], 0, v[132:133]
	v_lshl_add_u64 v[4:5], v[2:3], 0, s[38:39]
	global_load_lds_dwordx4 v[4:5], off
	v_lshl_add_u64 v[2:3], v[2:3], 0, s[40:41]
	s_add_i32 m0, s34, 0x2000
	s_nop 0
	global_load_lds_dwordx4 v[2:3], off
	s_mov_b32 m0, s73
	v_lshl_add_u64 v[2:3], s[60:61], 0, v[130:131]
	v_lshl_add_u64 v[4:5], v[2:3], 0, s[30:31]
	global_load_lds_dwordx4 v[4:5], off
	v_lshl_add_u64 v[2:3], v[2:3], 0, s[36:37]
	s_mov_b32 m0, s74
	s_nop 0
	global_load_lds_dwordx4 v[2:3], off
	s_waitcnt vmcnt(8)
	s_waitcnt lgkmcnt(0)
	s_barrier
	s_setprio 1
	s_waitcnt lgkmcnt(0)
	.p2align	4
	v_mfma_scale_f32_16x16x128_f8f6f4 v[38:41], v[98:105], v[114:121], v[38:41], v138, v138 op_sel_hi:[0,0,0]
	v_mfma_scale_f32_16x16x128_f8f6f4 v[34:37], v[106:113], v[114:121], v[34:37], v138, v138 op_sel_hi:[0,0,0]
	v_mfma_scale_f32_16x16x128_f8f6f4 v[30:33], v[98:105], v[148:155], v[208:211], v138, v138 op_sel_hi:[0,0,0]
	v_mfma_scale_f32_16x16x128_f8f6f4 v[26:29], v[106:113], v[148:155], v[212:215], v138, v138 op_sel_hi:[0,0,0]
	v_mfma_scale_f32_16x16x128_f8f6f4 v[22:25], v[98:105], v[156:163], v[216:219], v138, v138 op_sel_hi:[0,0,0]
	v_mfma_scale_f32_16x16x128_f8f6f4 v[220:223], v[106:113], v[156:163], v[220:223], v138, v138 op_sel_hi:[0,0,0]
	v_mfma_scale_f32_16x16x128_f8f6f4 v[2:5], v[98:105], v[164:171], v[224:227], v138, v138 op_sel_hi:[0,0,0]
	v_mfma_scale_f32_16x16x128_f8f6f4 v[10:13], v[106:113], v[164:171], v[228:231], v138, v138 op_sel_hi:[0,0,0]
	s_setprio 0
	s_setprio 1
	.p2align	4
	v_mfma_scale_f32_16x16x128_f8f6f4 v[98:101], v[122:129], v[114:121], v[232:235], v138, v138 op_sel_hi:[0,0,0]
	v_mfma_scale_f32_16x16x128_f8f6f4 v[102:105], v[140:147], v[114:121], v[236:239], v138, v138 op_sel_hi:[0,0,0]
	v_mfma_scale_f32_16x16x128_f8f6f4 v[106:109], v[122:129], v[148:155], v[240:243], v138, v138 op_sel_hi:[0,0,0]
	v_mfma_scale_f32_16x16x128_f8f6f4 v[110:113], v[140:147], v[148:155], v[244:247], v138, v138 op_sel_hi:[0,0,0]
	v_mfma_scale_f32_16x16x128_f8f6f4 v[114:117], v[122:129], v[156:163], v[248:251], v138, v138 op_sel_hi:[0,0,0]
	v_mfma_scale_f32_16x16x128_f8f6f4 v[118:121], v[140:147], v[156:163], v[42:45], v138, v138 op_sel_hi:[0,0,0]
	v_mfma_scale_f32_16x16x128_f8f6f4 v[122:125], v[122:129], v[164:171], v[46:49], v138, v138 op_sel_hi:[0,0,0]
	v_mfma_scale_f32_16x16x128_f8f6f4 v[126:129], v[140:147], v[164:171], v[50:53], v138, v138 op_sel_hi:[0,0,0]
	s_setprio 0
	s_barrier
	s_add_i32 s51, s51, 2
	s_add_u32 s58, s58, 0x100
	s_addc_u32 s59, s59, 0
	s_cmp_gt_u32 s51, 13
	s_cbranch_scc0 .LBB0_1224
	s_and_b64 vcc, exec, s[44:45]
	s_cbranch_vccz .LBB0_1227
	s_barrier

.LBB0_1257:
	s_add_u32 s60, s42, s54
	v_add_u32_e32 v42, s75, v1
	v_add_u32_e32 v43, s78, v42
	v_add_u32_e32 v42, s79, v42
	ds_read_b128 v[140:143], v43
	ds_read_b128 v[144:147], v43 offset:1024
	ds_read_b128 v[148:151], v43 offset:2048
	ds_read_b128 v[152:155], v43 offset:3072
	ds_read_b128 v[156:159], v42
	ds_read_b128 v[160:163], v42 offset:1024
	ds_read_b128 v[164:167], v42 offset:2048
	ds_read_b128 v[168:171], v42 offset:3072
	s_addc_u32 s61, s43, s55
	s_add_u32 s34, s60, 0x100
	s_addc_u32 s35, s61, 0
	s_add_u32 s58, s45, s54
	s_addc_u32 s59, s47, s55
	s_cmpk_eq_i32 s54, 0x700
	s_cselect_b32 s57, s51, s35
	s_cselect_b32 s56, s50, s34
	s_cselect_b32 s59, s53, s59
	s_cselect_b32 s58, s52, s58
	v_add_u32_e32 v42, s76, v1
	v_mov_b64_e32 v[46:47], v[172:173]
	v_mov_b64_e32 v[50:51], v[176:177]
	v_mov_b64_e32 v[48:49], v[174:175]
	ds_read_b128 v[172:175], v42
	v_mov_b64_e32 v[52:53], v[178:179]
	ds_read_b128 v[176:179], v42 offset:1024
	ds_read_b128 v[180:183], v42 offset:2048
	ds_read_b128 v[184:187], v42 offset:3072
	ds_read_b128 v[196:199], v42 offset:4096
	ds_read_b128 v[200:203], v42 offset:5120
	ds_read_b128 v[204:207], v42 offset:6144
	ds_read_b128 v[208:211], v42 offset:7168
	s_add_i32 m0, s23, 0xc000
	v_lshl_add_u64 v[42:43], s[60:61], 0, v[130:131]
	v_lshl_add_u64 v[44:45], v[42:43], 0, s[30:31]
	global_load_lds_dwordx4 v[44:45], off
	v_lshl_add_u64 v[42:43], v[42:43], 0, s[36:37]
	s_add_i32 m0, s23, 0xe000
	s_nop 0
	global_load_lds_dwordx4 v[42:43], off
	s_waitcnt vmcnt(8)
	s_waitcnt lgkmcnt(0)
	s_barrier
	s_setprio 1
	s_waitcnt lgkmcnt(0)
	.p2align	4
	v_mfma_scale_f32_16x16x128_f8f6f4 v[94:97], v[140:147], v[172:179], v[94:97], v138, v138 op_sel_hi:[0,0,0]
	v_mfma_scale_f32_16x16x128_f8f6f4 v[90:93], v[148:155], v[172:179], v[90:93], v138, v138 op_sel_hi:[0,0,0]
	v_mfma_scale_f32_16x16x128_f8f6f4 v[86:89], v[140:147], v[180:187], v[86:89], v138, v138 op_sel_hi:[0,0,0]
	v_mfma_scale_f32_16x16x128_f8f6f4 v[82:85], v[148:155], v[180:187], v[82:85], v138, v138 op_sel_hi:[0,0,0]
	v_mfma_scale_f32_16x16x128_f8f6f4 v[78:81], v[140:147], v[196:203], v[78:81], v138, v138 op_sel_hi:[0,0,0]
	v_mfma_scale_f32_16x16x128_f8f6f4 v[74:77], v[148:155], v[196:203], v[74:77], v138, v138 op_sel_hi:[0,0,0]
	v_mfma_scale_f32_16x16x128_f8f6f4 v[134:137], v[140:147], v[204:211], v[70:73], v138, v138 op_sel_hi:[0,0,0]
	v_mfma_scale_f32_16x16x128_f8f6f4 v[188:191], v[148:155], v[204:211], v[66:69], v138, v138 op_sel_hi:[0,0,0]
	s_setprio 0
	s_setprio 1
	.p2align	4
	v_mfma_scale_f32_16x16x128_f8f6f4 v[192:195], v[156:163], v[172:179], v[62:65], v138, v138 op_sel_hi:[0,0,0]
	v_mfma_scale_f32_16x16x128_f8f6f4 v[172:175], v[164:171], v[172:179], v[58:61], v138, v138 op_sel_hi:[0,0,0]
	v_mfma_scale_f32_16x16x128_f8f6f4 v[176:179], v[156:163], v[180:187], v[54:57], v138, v138 op_sel_hi:[0,0,0]
	v_mfma_scale_f32_16x16x128_f8f6f4 v[180:183], v[164:171], v[180:187], v[50:53], v138, v138 op_sel_hi:[0,0,0]
	v_mfma_scale_f32_16x16x128_f8f6f4 v[184:187], v[156:163], v[196:203], v[46:49], v138, v138 op_sel_hi:[0,0,0]
	v_mfma_scale_f32_16x16x128_f8f6f4 v[196:199], v[164:171], v[196:203], v[18:21], v138, v138 op_sel_hi:[0,0,0]
	v_mfma_scale_f32_16x16x128_f8f6f4 v[200:203], v[156:163], v[204:211], v[6:9], v138, v138 op_sel_hi:[0,0,0]
	v_mfma_scale_f32_16x16x128_f8f6f4 v[204:207], v[164:171], v[204:211], v[14:17], v138, v138 op_sel_hi:[0,0,0]
	s_setprio 0
	s_barrier
	v_mov_b32_e32 v133, v131
	s_nop 2
	v_add_u32_e32 v6, s76, v1
	s_add_i32 s34, s78, s39
	ds_read_b128 v[42:45], v6 offset:16384
	ds_read_b128 v[46:49], v6 offset:17408
	ds_read_b128 v[50:53], v6 offset:18432
	ds_read_b128 v[54:57], v6 offset:19456
	ds_read_b128 v[58:61], v6 offset:20480
	ds_read_b128 v[62:65], v6 offset:21504
	ds_read_b128 v[66:69], v6 offset:22528
	ds_read_b128 v[70:73], v6 offset:23552
	s_mov_b32 m0, s34
	v_lshl_add_u64 v[6:7], s[58:59], 0, v[132:133]
	global_load_lds_dwordx4 v132, s[58:59]
	v_lshl_add_u64 v[6:7], v[6:7], 0, s[8:9]
	s_add_i32 m0, s34, 0x2000
	s_add_i32 s34, s79, s39
	global_load_lds_dwordx4 v[6:7], off
	s_mov_b32 m0, s34
	v_lshl_add_u64 v[6:7], s[58:59], 0, v[132:133]
	v_lshl_add_u64 v[8:9], v[6:7], 0, s[18:19]
	global_load_lds_dwordx4 v[8:9], off
	v_lshl_add_u64 v[6:7], v[6:7], 0, s[20:21]
	s_add_i32 m0, s34, 0x2000
	s_nop 0
	global_load_lds_dwordx4 v[6:7], off
	s_mov_b32 m0, s23
	v_lshl_add_u64 v[6:7], s[56:57], 0, v[130:131]
	global_load_lds_dwordx4 v130, s[56:57]
	v_lshl_add_u64 v[6:7], v[6:7], 0, s[8:9]
	s_mov_b32 m0, s69
	s_nop 0
	global_load_lds_dwordx4 v[6:7], off
	s_waitcnt vmcnt(8)
	s_waitcnt lgkmcnt(0)
	s_barrier
	s_setprio 1
	s_waitcnt lgkmcnt(0)
	.p2align	4
	v_mfma_scale_f32_16x16x128_f8f6f4 v[38:41], v[140:147], v[42:49], v[38:41], v138, v138 op_sel_hi:[0,0,0]
	v_mfma_scale_f32_16x16x128_f8f6f4 v[34:37], v[148:155], v[42:49], v[34:37], v138, v138 op_sel_hi:[0,0,0]
	v_mfma_scale_f32_16x16x128_f8f6f4 v[220:223], v[148:155], v[58:65], v[220:223], v138, v138 op_sel_hi:[0,0,0]
	v_mfma_scale_f32_16x16x128_f8f6f4 v[208:211], v[140:147], v[50:57], v[30:33], v138, v138 op_sel_hi:[0,0,0]
	v_mfma_scale_f32_16x16x128_f8f6f4 v[212:215], v[148:155], v[50:57], v[26:29], v138, v138 op_sel_hi:[0,0,0]
	v_mfma_scale_f32_16x16x128_f8f6f4 v[216:219], v[140:147], v[58:65], v[22:25], v138, v138 op_sel_hi:[0,0,0]
	v_mfma_scale_f32_16x16x128_f8f6f4 v[224:227], v[140:147], v[66:73], v[2:5], v138, v138 op_sel_hi:[0,0,0]
	v_mfma_scale_f32_16x16x128_f8f6f4 v[228:231], v[148:155], v[66:73], v[10:13], v138, v138 op_sel_hi:[0,0,0]
	s_setprio 0
	s_setprio 1
	.p2align	4
	v_mfma_scale_f32_16x16x128_f8f6f4 v[232:235], v[156:163], v[42:49], v[98:101], v138, v138 op_sel_hi:[0,0,0]
	v_mfma_scale_f32_16x16x128_f8f6f4 v[236:239], v[164:171], v[42:49], v[102:105], v138, v138 op_sel_hi:[0,0,0]
	v_mfma_scale_f32_16x16x128_f8f6f4 v[240:243], v[156:163], v[50:57], v[106:109], v138, v138 op_sel_hi:[0,0,0]
	v_mfma_scale_f32_16x16x128_f8f6f4 v[244:247], v[164:171], v[50:57], v[110:113], v138, v138 op_sel_hi:[0,0,0]
	v_mfma_scale_f32_16x16x128_f8f6f4 v[248:251], v[156:163], v[58:65], v[114:117], v138, v138 op_sel_hi:[0,0,0]
	v_mfma_scale_f32_16x16x128_f8f6f4 v[42:45], v[164:171], v[58:65], v[118:121], v138, v138 op_sel_hi:[0,0,0]
	v_mfma_scale_f32_16x16x128_f8f6f4 v[46:49], v[156:163], v[66:73], v[122:125], v138, v138 op_sel_hi:[0,0,0]
	v_mfma_scale_f32_16x16x128_f8f6f4 v[50:53], v[164:171], v[66:73], v[126:129], v138, v138 op_sel_hi:[0,0,0]
	s_setprio 0
	s_barrier
	s_add_i32 s34, 0, 0x18000
	v_add_u32_e32 v2, s75, v1
	s_add_i32 s35, 0, 0x1c000
	v_add_u32_e32 v3, s34, v2
	v_add_u32_e32 v2, s35, v2
	ds_read_b128 v[98:101], v3
	ds_read_b128 v[102:105], v3 offset:1024
	ds_read_b128 v[106:109], v3 offset:2048
	ds_read_b128 v[110:113], v3 offset:3072
	ds_read_b128 v[122:125], v2
	ds_read_b128 v[126:129], v2 offset:1024
	ds_read_b128 v[140:143], v2 offset:2048
	ds_read_b128 v[144:147], v2 offset:3072
	v_add_u32_e32 v30, s76, v1
	ds_read_b128 v[2:5], v30 offset:32768
	ds_read_b128 v[6:9], v30 offset:33792
	ds_read_b128 v[10:13], v30 offset:34816
	ds_read_b128 v[14:17], v30 offset:35840
	ds_read_b128 v[18:21], v30 offset:36864
	ds_read_b128 v[22:25], v30 offset:37888
	ds_read_b128 v[26:29], v30 offset:38912
	ds_read_b128 v[30:33], v30 offset:39936
	s_mov_b32 m0, s70
	v_lshl_add_u64 v[54:55], s[56:57], 0, v[130:131]
	v_lshl_add_u64 v[56:57], v[54:55], 0, s[18:19]
	global_load_lds_dwordx4 v[56:57], off
	v_lshl_add_u64 v[54:55], v[54:55], 0, s[20:21]
	s_mov_b32 m0, s71
	s_nop 0
	global_load_lds_dwordx4 v[54:55], off
	s_waitcnt vmcnt(8)
	s_waitcnt lgkmcnt(0)
	s_barrier
	s_setprio 1
	s_waitcnt lgkmcnt(0)
	.p2align	4
	v_mfma_scale_f32_16x16x128_f8f6f4 v[94:97], v[98:105], v[2:9], v[94:97], v138, v138 op_sel_hi:[0,0,0]
	v_mfma_scale_f32_16x16x128_f8f6f4 v[90:93], v[106:113], v[2:9], v[90:93], v138, v138 op_sel_hi:[0,0,0]
	v_mfma_scale_f32_16x16x128_f8f6f4 v[86:89], v[98:105], v[10:17], v[86:89], v138, v138 op_sel_hi:[0,0,0]
	v_mfma_scale_f32_16x16x128_f8f6f4 v[82:85], v[106:113], v[10:17], v[82:85], v138, v138 op_sel_hi:[0,0,0]
	v_mfma_scale_f32_16x16x128_f8f6f4 v[78:81], v[98:105], v[18:25], v[78:81], v138, v138 op_sel_hi:[0,0,0]
	v_mfma_scale_f32_16x16x128_f8f6f4 v[74:77], v[106:113], v[18:25], v[74:77], v138, v138 op_sel_hi:[0,0,0]
	v_mfma_scale_f32_16x16x128_f8f6f4 v[70:73], v[98:105], v[26:33], v[134:137], v138, v138 op_sel_hi:[0,0,0]
	v_mfma_scale_f32_16x16x128_f8f6f4 v[66:69], v[106:113], v[26:33], v[188:191], v138, v138 op_sel_hi:[0,0,0]
	s_setprio 0
	s_setprio 1
	.p2align	4
	v_mfma_scale_f32_16x16x128_f8f6f4 v[62:65], v[122:129], v[2:9], v[192:195], v138, v138 op_sel_hi:[0,0,0]
	v_mfma_scale_f32_16x16x128_f8f6f4 v[58:61], v[140:147], v[2:9], v[172:175], v138, v138 op_sel_hi:[0,0,0]
	v_mfma_scale_f32_16x16x128_f8f6f4 v[54:57], v[122:129], v[10:17], v[176:179], v138, v138 op_sel_hi:[0,0,0]
	v_mfma_scale_f32_16x16x128_f8f6f4 v[176:179], v[140:147], v[10:17], v[180:183], v138, v138 op_sel_hi:[0,0,0]
	v_mfma_scale_f32_16x16x128_f8f6f4 v[172:175], v[122:129], v[18:25], v[184:187], v138, v138 op_sel_hi:[0,0,0]
	v_mfma_scale_f32_16x16x128_f8f6f4 v[18:21], v[140:147], v[18:25], v[196:199], v138, v138 op_sel_hi:[0,0,0]
	v_mfma_scale_f32_16x16x128_f8f6f4 v[6:9], v[122:129], v[26:33], v[200:203], v138, v138 op_sel_hi:[0,0,0]
	v_mfma_scale_f32_16x16x128_f8f6f4 v[14:17], v[140:147], v[26:33], v[204:207], v138, v138 op_sel_hi:[0,0,0]
	s_setprio 0
	s_barrier
	s_add_i32 s34, s34, s39
	v_add_u32_e32 v2, s76, v1
	ds_read_b128 v[114:117], v2 offset:49152
	ds_read_b128 v[118:121], v2 offset:50176
	ds_read_b128 v[148:151], v2 offset:51200
	ds_read_b128 v[152:155], v2 offset:52224
	ds_read_b128 v[156:159], v2 offset:53248
	ds_read_b128 v[160:163], v2 offset:54272
	ds_read_b128 v[164:167], v2 offset:55296
	ds_read_b128 v[168:171], v2 offset:56320
	s_mov_b32 m0, s34
	v_lshl_add_u64 v[2:3], s[58:59], 0, v[132:133]
	v_lshl_add_u64 v[4:5], v[2:3], 0, s[26:27]
	global_load_lds_dwordx4 v[4:5], off
	v_lshl_add_u64 v[2:3], v[2:3], 0, s[28:29]
	s_add_i32 m0, s34, 0x2000
	s_add_i32 s34, s35, s39
	global_load_lds_dwordx4 v[2:3], off
	s_mov_b32 m0, s34
	v_lshl_add_u64 v[2:3], s[58:59], 0, v[132:133]
	v_lshl_add_u64 v[4:5], v[2:3], 0, s[30:31]
	global_load_lds_dwordx4 v[4:5], off
	v_lshl_add_u64 v[2:3], v[2:3], 0, s[36:37]
	s_add_i32 m0, s34, 0x2000
	s_nop 0
	global_load_lds_dwordx4 v[2:3], off
	s_mov_b32 m0, s72
	v_lshl_add_u64 v[2:3], s[56:57], 0, v[130:131]
	v_lshl_add_u64 v[4:5], v[2:3], 0, s[26:27]
	global_load_lds_dwordx4 v[4:5], off
	v_lshl_add_u64 v[2:3], v[2:3], 0, s[28:29]
	s_mov_b32 m0, s73
	s_nop 0
	global_load_lds_dwordx4 v[2:3], off
	s_waitcnt vmcnt(8)
	s_waitcnt lgkmcnt(0)
	s_barrier
	s_setprio 1
	s_waitcnt lgkmcnt(0)
	.p2align	4
	v_mfma_scale_f32_16x16x128_f8f6f4 v[38:41], v[98:105], v[114:121], v[38:41], v138, v138 op_sel_hi:[0,0,0]
	v_mfma_scale_f32_16x16x128_f8f6f4 v[34:37], v[106:113], v[114:121], v[34:37], v138, v138 op_sel_hi:[0,0,0]
	v_mfma_scale_f32_16x16x128_f8f6f4 v[30:33], v[98:105], v[148:155], v[208:211], v138, v138 op_sel_hi:[0,0,0]
	v_mfma_scale_f32_16x16x128_f8f6f4 v[26:29], v[106:113], v[148:155], v[212:215], v138, v138 op_sel_hi:[0,0,0]
	v_mfma_scale_f32_16x16x128_f8f6f4 v[22:25], v[98:105], v[156:163], v[216:219], v138, v138 op_sel_hi:[0,0,0]
	v_mfma_scale_f32_16x16x128_f8f6f4 v[220:223], v[106:113], v[156:163], v[220:223], v138, v138 op_sel_hi:[0,0,0]
	v_mfma_scale_f32_16x16x128_f8f6f4 v[2:5], v[98:105], v[164:171], v[224:227], v138, v138 op_sel_hi:[0,0,0]
	v_mfma_scale_f32_16x16x128_f8f6f4 v[10:13], v[106:113], v[164:171], v[228:231], v138, v138 op_sel_hi:[0,0,0]
	s_setprio 0
	s_setprio 1
	.p2align	4
	v_mfma_scale_f32_16x16x128_f8f6f4 v[98:101], v[122:129], v[114:121], v[232:235], v138, v138 op_sel_hi:[0,0,0]
	v_mfma_scale_f32_16x16x128_f8f6f4 v[102:105], v[140:147], v[114:121], v[236:239], v138, v138 op_sel_hi:[0,0,0]
	v_mfma_scale_f32_16x16x128_f8f6f4 v[106:109], v[122:129], v[148:155], v[240:243], v138, v138 op_sel_hi:[0,0,0]
	v_mfma_scale_f32_16x16x128_f8f6f4 v[110:113], v[140:147], v[148:155], v[244:247], v138, v138 op_sel_hi:[0,0,0]
	v_mfma_scale_f32_16x16x128_f8f6f4 v[114:117], v[122:129], v[156:163], v[248:251], v138, v138 op_sel_hi:[0,0,0]
	v_mfma_scale_f32_16x16x128_f8f6f4 v[118:121], v[140:147], v[156:163], v[42:45], v138, v138 op_sel_hi:[0,0,0]
	v_mfma_scale_f32_16x16x128_f8f6f4 v[122:125], v[122:129], v[164:171], v[46:49], v138, v138 op_sel_hi:[0,0,0]
	v_mfma_scale_f32_16x16x128_f8f6f4 v[126:129], v[140:147], v[164:171], v[50:53], v138, v138 op_sel_hi:[0,0,0]
	s_setprio 0
	s_barrier
	s_add_i32 s86, s86, 2
	s_add_u32 s54, s54, 0x100
	s_addc_u32 s55, s55, 0
	s_cmp_gt_u32 s86, 13
	s_cbranch_scc0 .LBB0_1257
	s_and_b64 vcc, exec, s[40:41]
	s_cbranch_vccz .LBB0_1260
	s_barrier

.LBB0_1308:
	s_add_u32 s34, s4, 0xfffa0080
	v_add_u32_e32 v133, s71, v1
	v_add_u32_e32 v148, s74, v133
	v_add_u32_e32 v133, s75, v133
	ds_read_b128 v[136:139], v148
	ds_read_b128 v[140:143], v148 offset:1024
	ds_read_b128 v[144:147], v148 offset:2048
	ds_read_b128 v[148:151], v148 offset:3072
	ds_read_b128 v[152:155], v133
	ds_read_b128 v[156:159], v133 offset:1024
	ds_read_b128 v[160:163], v133 offset:2048
	ds_read_b128 v[164:167], v133 offset:3072
	s_addc_u32 s35, s5, -1
	s_cmp_eq_u32 s83, 12
	s_cselect_b32 s53, s45, s35
	s_cselect_b32 s52, s44, s34
	s_cselect_b32 s55, s47, s43
	s_cselect_b32 s54, s46, s41
	v_add_u32_e32 v133, s72, v1
	s_mov_b32 s34, 0xfffe0000
	ds_read_b128 v[168:171], v133
	ds_read_b128 v[172:175], v133 offset:1024
	ds_read_b128 v[176:179], v133 offset:2048
	ds_read_b128 v[180:183], v133 offset:3072
	ds_read_b128 v[184:187], v133 offset:4096
	ds_read_b128 v[188:191], v133 offset:5120
	ds_read_b128 v[196:199], v133 offset:6144
	ds_read_b128 v[200:203], v133 offset:7168
	s_mov_b32 s35, -1
	v_lshl_add_u64 v[192:193], s[4:5], 0, v[130:131]
	v_lshl_add_u64 v[192:193], v[192:193], 0, s[34:35]
	s_add_i32 m0, s51, 0xc000
	s_nop 0
	global_load_lds_dwordx4 v[192:193], off
	s_add_i32 m0, s51, 0xe000
	s_nop 0
	global_load_lds_dwordx4 v130, s[4:5]
	s_waitcnt vmcnt(8)
	s_waitcnt lgkmcnt(0)
	s_barrier
	s_setprio 1
	s_waitcnt lgkmcnt(0)
	.p2align	4
	v_mfma_scale_f32_16x16x128_f8f6f4 v[126:129], v[136:143], v[168:175], v[126:129], v134, v134 op_sel_hi:[0,0,0]
	v_mfma_scale_f32_16x16x128_f8f6f4 v[122:125], v[144:151], v[168:175], v[122:125], v134, v134 op_sel_hi:[0,0,0]
	v_mfma_scale_f32_16x16x128_f8f6f4 v[110:113], v[136:143], v[176:183], v[110:113], v134, v134 op_sel_hi:[0,0,0]
	v_mfma_scale_f32_16x16x128_f8f6f4 v[106:109], v[144:151], v[176:183], v[106:109], v134, v134 op_sel_hi:[0,0,0]
	v_mfma_scale_f32_16x16x128_f8f6f4 v[192:195], v[136:143], v[184:191], v[94:97], v134, v134 op_sel_hi:[0,0,0]
	v_mfma_scale_f32_16x16x128_f8f6f4 v[204:207], v[144:151], v[184:191], v[90:93], v134, v134 op_sel_hi:[0,0,0]
	v_mfma_scale_f32_16x16x128_f8f6f4 v[208:211], v[136:143], v[196:203], v[78:81], v134, v134 op_sel_hi:[0,0,0]
	v_mfma_scale_f32_16x16x128_f8f6f4 v[212:215], v[144:151], v[196:203], v[74:77], v134, v134 op_sel_hi:[0,0,0]
	s_setprio 0
	s_setprio 1
	.p2align	4
	v_mfma_scale_f32_16x16x128_f8f6f4 v[118:121], v[152:159], v[168:175], v[118:121], v134, v134 op_sel_hi:[0,0,0]
	v_mfma_scale_f32_16x16x128_f8f6f4 v[114:117], v[160:167], v[168:175], v[114:117], v134, v134 op_sel_hi:[0,0,0]
	v_mfma_scale_f32_16x16x128_f8f6f4 v[102:105], v[152:159], v[176:183], v[102:105], v134, v134 op_sel_hi:[0,0,0]
	v_mfma_scale_f32_16x16x128_f8f6f4 v[98:101], v[160:167], v[176:183], v[98:101], v134, v134 op_sel_hi:[0,0,0]
	v_mfma_scale_f32_16x16x128_f8f6f4 v[168:171], v[152:159], v[184:191], v[86:89], v134, v134 op_sel_hi:[0,0,0]
	v_mfma_scale_f32_16x16x128_f8f6f4 v[172:175], v[160:167], v[184:191], v[82:85], v134, v134 op_sel_hi:[0,0,0]
	v_mfma_scale_f32_16x16x128_f8f6f4 v[176:179], v[152:159], v[196:203], v[66:69], v134, v134 op_sel_hi:[0,0,0]
	v_mfma_scale_f32_16x16x128_f8f6f4 v[180:183], v[160:167], v[196:203], v[70:73], v134, v134 op_sel_hi:[0,0,0]
	s_setprio 0
	s_barrier
	v_mov_b32_e32 v133, v131
	v_add_u32_e32 v94, s72, v1
	s_add_i32 s34, s74, s62
	s_nop 0
	ds_read_b128 v[66:69], v94 offset:16384
	ds_read_b128 v[70:73], v94 offset:17408
	ds_read_b128 v[74:77], v94 offset:18432
	ds_read_b128 v[78:81], v94 offset:19456
	ds_read_b128 v[82:85], v94 offset:20480
	ds_read_b128 v[86:89], v94 offset:21504
	ds_read_b128 v[90:93], v94 offset:22528
	ds_read_b128 v[94:97], v94 offset:23552
	s_mov_b32 m0, s34
	v_lshl_add_u64 v[184:185], s[54:55], 0, v[132:133]
	global_load_lds_dwordx4 v132, s[54:55]
	v_lshl_add_u64 v[184:185], v[184:185], 0, s[8:9]
	s_add_i32 m0, s34, 0x2000
	s_add_i32 s34, s75, s62
	global_load_lds_dwordx4 v[184:185], off
	s_mov_b32 m0, s34
	v_lshl_add_u64 v[184:185], s[54:55], 0, v[132:133]
	v_lshl_add_u64 v[186:187], v[184:185], 0, s[12:13]
	global_load_lds_dwordx4 v[186:187], off
	v_lshl_add_u64 v[184:185], v[184:185], 0, s[14:15]
	s_add_i32 m0, s34, 0x2000
	s_nop 0
	global_load_lds_dwordx4 v[184:185], off
	s_mov_b32 m0, s51
	v_lshl_add_u64 v[184:185], s[52:53], 0, v[130:131]
	global_load_lds_dwordx4 v130, s[52:53]
	v_lshl_add_u64 v[184:185], v[184:185], 0, s[8:9]
	s_mov_b32 m0, s64
	s_nop 0
	global_load_lds_dwordx4 v[184:185], off
	s_waitcnt vmcnt(8)
	s_waitcnt lgkmcnt(0)
	s_barrier
	s_setprio 1
	s_waitcnt lgkmcnt(0)
	.p2align	4
	v_mfma_scale_f32_16x16x128_f8f6f4 v[62:65], v[136:143], v[66:73], v[62:65], v134, v134 op_sel_hi:[0,0,0]
	v_mfma_scale_f32_16x16x128_f8f6f4 v[58:61], v[144:151], v[66:73], v[58:61], v134, v134 op_sel_hi:[0,0,0]
	v_mfma_scale_f32_16x16x128_f8f6f4 v[10:13], v[136:143], v[90:97], v[10:13], v134, v134 op_sel_hi:[0,0,0]
	v_mfma_scale_f32_16x16x128_f8f6f4 v[184:187], v[136:143], v[74:81], v[46:49], v134, v134 op_sel_hi:[0,0,0]
	v_mfma_scale_f32_16x16x128_f8f6f4 v[188:191], v[144:151], v[74:81], v[42:45], v134, v134 op_sel_hi:[0,0,0]
	v_mfma_scale_f32_16x16x128_f8f6f4 v[196:199], v[136:143], v[82:89], v[30:33], v134, v134 op_sel_hi:[0,0,0]
	v_mfma_scale_f32_16x16x128_f8f6f4 v[200:203], v[144:151], v[82:89], v[26:29], v134, v134 op_sel_hi:[0,0,0]
	v_mfma_scale_f32_16x16x128_f8f6f4 v[216:219], v[144:151], v[90:97], v[14:17], v134, v134 op_sel_hi:[0,0,0]
	s_setprio 0
	s_setprio 1
	.p2align	4
	v_mfma_scale_f32_16x16x128_f8f6f4 v[54:57], v[152:159], v[66:73], v[54:57], v134, v134 op_sel_hi:[0,0,0]
	v_mfma_scale_f32_16x16x128_f8f6f4 v[220:223], v[160:167], v[66:73], v[50:53], v134, v134 op_sel_hi:[0,0,0]
	v_mfma_scale_f32_16x16x128_f8f6f4 v[224:227], v[152:159], v[74:81], v[38:41], v134, v134 op_sel_hi:[0,0,0]
	v_mfma_scale_f32_16x16x128_f8f6f4 v[228:231], v[160:167], v[74:81], v[34:37], v134, v134 op_sel_hi:[0,0,0]
	v_mfma_scale_f32_16x16x128_f8f6f4 v[232:235], v[152:159], v[82:89], v[22:25], v134, v134 op_sel_hi:[0,0,0]
	v_mfma_scale_f32_16x16x128_f8f6f4 v[236:239], v[160:167], v[82:89], v[18:21], v134, v134 op_sel_hi:[0,0,0]
	v_mfma_scale_f32_16x16x128_f8f6f4 v[240:243], v[152:159], v[90:97], v[6:9], v134, v134 op_sel_hi:[0,0,0]
	v_mfma_scale_f32_16x16x128_f8f6f4 v[244:247], v[160:167], v[90:97], v[2:5], v134, v134 op_sel_hi:[0,0,0]
	s_setprio 0
	s_barrier
	s_add_i32 s34, 0, 0x18000
	s_nop 0
	v_add_u32_e32 v22, s71, v1
	s_add_i32 s35, 0, 0x1c000
	v_add_u32_e32 v18, s34, v22
	v_add_u32_e32 v22, s35, v22
	ds_read_b128 v[2:5], v18
	ds_read_b128 v[6:9], v18 offset:1024
	ds_read_b128 v[14:17], v18 offset:2048
	ds_read_b128 v[18:21], v18 offset:3072
	ds_read_b128 v[136:139], v22
	ds_read_b128 v[140:143], v22 offset:1024
	ds_read_b128 v[144:147], v22 offset:2048
	ds_read_b128 v[148:151], v22 offset:3072
	v_add_u32_e32 v50, s72, v1
	ds_read_b128 v[22:25], v50 offset:32768
	ds_read_b128 v[26:29], v50 offset:33792
	ds_read_b128 v[30:33], v50 offset:34816
	ds_read_b128 v[34:37], v50 offset:35840
	ds_read_b128 v[38:41], v50 offset:36864
	ds_read_b128 v[42:45], v50 offset:37888
	ds_read_b128 v[46:49], v50 offset:38912
	ds_read_b128 v[50:53], v50 offset:39936
	s_mov_b32 m0, s65
	v_lshl_add_u64 v[66:67], s[52:53], 0, v[130:131]
	v_lshl_add_u64 v[68:69], v[66:67], 0, s[12:13]
	global_load_lds_dwordx4 v[68:69], off
	v_lshl_add_u64 v[66:67], v[66:67], 0, s[14:15]
	s_mov_b32 m0, s66
	s_nop 0
	global_load_lds_dwordx4 v[66:67], off
	s_waitcnt vmcnt(8)
	s_waitcnt lgkmcnt(0)
	s_barrier
	s_setprio 1
	s_waitcnt lgkmcnt(0)
	.p2align	4
	v_mfma_scale_f32_16x16x128_f8f6f4 v[126:129], v[2:9], v[22:29], v[126:129], v134, v134 op_sel_hi:[0,0,0]
	v_mfma_scale_f32_16x16x128_f8f6f4 v[122:125], v[14:21], v[22:29], v[122:125], v134, v134 op_sel_hi:[0,0,0]
	v_mfma_scale_f32_16x16x128_f8f6f4 v[110:113], v[2:9], v[30:37], v[110:113], v134, v134 op_sel_hi:[0,0,0]
	v_mfma_scale_f32_16x16x128_f8f6f4 v[106:109], v[14:21], v[30:37], v[106:109], v134, v134 op_sel_hi:[0,0,0]
	v_mfma_scale_f32_16x16x128_f8f6f4 v[94:97], v[2:9], v[38:45], v[192:195], v134, v134 op_sel_hi:[0,0,0]
	v_mfma_scale_f32_16x16x128_f8f6f4 v[90:93], v[14:21], v[38:45], v[204:207], v134, v134 op_sel_hi:[0,0,0]
	v_mfma_scale_f32_16x16x128_f8f6f4 v[78:81], v[2:9], v[46:53], v[208:211], v134, v134 op_sel_hi:[0,0,0]
	v_mfma_scale_f32_16x16x128_f8f6f4 v[74:77], v[14:21], v[46:53], v[212:215], v134, v134 op_sel_hi:[0,0,0]
	s_setprio 0
	s_setprio 1
	.p2align	4
	v_mfma_scale_f32_16x16x128_f8f6f4 v[118:121], v[136:143], v[22:29], v[118:121], v134, v134 op_sel_hi:[0,0,0]
	v_mfma_scale_f32_16x16x128_f8f6f4 v[114:117], v[144:151], v[22:29], v[114:117], v134, v134 op_sel_hi:[0,0,0]
	v_mfma_scale_f32_16x16x128_f8f6f4 v[102:105], v[136:143], v[30:37], v[102:105], v134, v134 op_sel_hi:[0,0,0]
	v_mfma_scale_f32_16x16x128_f8f6f4 v[98:101], v[144:151], v[30:37], v[98:101], v134, v134 op_sel_hi:[0,0,0]
	v_mfma_scale_f32_16x16x128_f8f6f4 v[86:89], v[136:143], v[38:45], v[168:171], v134, v134 op_sel_hi:[0,0,0]
	v_mfma_scale_f32_16x16x128_f8f6f4 v[82:85], v[144:151], v[38:45], v[172:175], v134, v134 op_sel_hi:[0,0,0]
	v_mfma_scale_f32_16x16x128_f8f6f4 v[66:69], v[136:143], v[46:53], v[176:179], v134, v134 op_sel_hi:[0,0,0]
	v_mfma_scale_f32_16x16x128_f8f6f4 v[70:73], v[144:151], v[46:53], v[180:183], v134, v134 op_sel_hi:[0,0,0]
	s_setprio 0
	s_barrier
	s_add_i32 s34, s34, s62
	v_add_u32_e32 v22, s72, v1
	ds_read_b128 v[34:37], v22 offset:49152
	ds_read_b128 v[38:41], v22 offset:50176
	ds_read_b128 v[152:155], v22 offset:51200
	ds_read_b128 v[156:159], v22 offset:52224
	ds_read_b128 v[160:163], v22 offset:53248
	ds_read_b128 v[164:167], v22 offset:54272
	ds_read_b128 v[168:171], v22 offset:55296
	ds_read_b128 v[172:175], v22 offset:56320
	s_mov_b32 m0, s34
	v_lshl_add_u64 v[22:23], s[54:55], 0, v[132:133]
	v_lshl_add_u64 v[24:25], v[22:23], 0, s[20:21]
	global_load_lds_dwordx4 v[24:25], off
	v_lshl_add_u64 v[22:23], v[22:23], 0, s[22:23]
	s_add_i32 m0, s34, 0x2000
	s_add_i32 s34, s35, s62
	global_load_lds_dwordx4 v[22:23], off
	s_mov_b32 m0, s34
	v_lshl_add_u64 v[22:23], s[54:55], 0, v[132:133]
	v_lshl_add_u64 v[24:25], v[22:23], 0, s[24:25]
	global_load_lds_dwordx4 v[24:25], off
	v_lshl_add_u64 v[22:23], v[22:23], 0, s[26:27]
	s_add_i32 m0, s34, 0x2000
	s_nop 0
	global_load_lds_dwordx4 v[22:23], off
	s_mov_b32 m0, s69
	v_lshl_add_u64 v[22:23], s[52:53], 0, v[130:131]
	v_lshl_add_u64 v[24:25], v[22:23], 0, s[20:21]
	global_load_lds_dwordx4 v[24:25], off
	v_lshl_add_u64 v[22:23], v[22:23], 0, s[22:23]
	s_mov_b32 m0, s70
	s_nop 0
	global_load_lds_dwordx4 v[22:23], off
	s_waitcnt vmcnt(8)
	s_waitcnt lgkmcnt(0)
	s_barrier
	s_setprio 1
	s_waitcnt lgkmcnt(0)
	.p2align	4
	v_mfma_scale_f32_16x16x128_f8f6f4 v[62:65], v[2:9], v[34:41], v[62:65], v134, v134 op_sel_hi:[0,0,0]
	v_mfma_scale_f32_16x16x128_f8f6f4 v[58:61], v[14:21], v[34:41], v[58:61], v134, v134 op_sel_hi:[0,0,0]
	v_mfma_scale_f32_16x16x128_f8f6f4 v[46:49], v[2:9], v[152:159], v[184:187], v134, v134 op_sel_hi:[0,0,0]
	v_mfma_scale_f32_16x16x128_f8f6f4 v[42:45], v[14:21], v[152:159], v[188:191], v134, v134 op_sel_hi:[0,0,0]
	v_mfma_scale_f32_16x16x128_f8f6f4 v[30:33], v[2:9], v[160:167], v[196:199], v134, v134 op_sel_hi:[0,0,0]
	v_mfma_scale_f32_16x16x128_f8f6f4 v[26:29], v[14:21], v[160:167], v[200:203], v134, v134 op_sel_hi:[0,0,0]
	v_mfma_scale_f32_16x16x128_f8f6f4 v[10:13], v[2:9], v[168:175], v[10:13], v134, v134 op_sel_hi:[0,0,0]
	v_mfma_scale_f32_16x16x128_f8f6f4 v[14:17], v[14:21], v[168:175], v[216:219], v134, v134 op_sel_hi:[0,0,0]
	s_setprio 0
	s_setprio 1
	.p2align	4
	v_mfma_scale_f32_16x16x128_f8f6f4 v[54:57], v[136:143], v[34:41], v[54:57], v134, v134 op_sel_hi:[0,0,0]
	v_mfma_scale_f32_16x16x128_f8f6f4 v[50:53], v[144:151], v[34:41], v[220:223], v134, v134 op_sel_hi:[0,0,0]
	v_mfma_scale_f32_16x16x128_f8f6f4 v[38:41], v[136:143], v[152:159], v[224:227], v134, v134 op_sel_hi:[0,0,0]
	v_mfma_scale_f32_16x16x128_f8f6f4 v[34:37], v[144:151], v[152:159], v[228:231], v134, v134 op_sel_hi:[0,0,0]
	v_mfma_scale_f32_16x16x128_f8f6f4 v[22:25], v[136:143], v[160:167], v[232:235], v134, v134 op_sel_hi:[0,0,0]
	v_mfma_scale_f32_16x16x128_f8f6f4 v[18:21], v[144:151], v[160:167], v[236:239], v134, v134 op_sel_hi:[0,0,0]
	v_mfma_scale_f32_16x16x128_f8f6f4 v[6:9], v[136:143], v[168:175], v[240:243], v134, v134 op_sel_hi:[0,0,0]
	v_mfma_scale_f32_16x16x128_f8f6f4 v[2:5], v[144:151], v[168:175], v[244:247], v134, v134 op_sel_hi:[0,0,0]
	s_setprio 0
	s_barrier
	s_add_i32 s83, s83, 2
	s_add_u32 s4, s4, 0x100
	s_addc_u32 s5, s5, 0
	s_add_u32 s41, s41, 0x100
	s_addc_u32 s43, s43, 0
	s_cmp_gt_u32 s83, 13
	s_cbranch_scc0 .LBB0_1308
	s_and_b64 vcc, exec, s[28:29]
	s_cbranch_vccz .LBB0_1311
	s_barrier
